# GEMM epilogues: out-proj residual pieces and in-proj rotary table pieces prefetched four 16-row groups ahead with counted waits (no per-step full drains)
# baseline (speedup 1.0000x reference)
;     __device__ __forceinline__ void operator()(const f32x4 (&acc)[2][2][4][2], const Unit& u, int wr, int wc, int fr, int fq) const {
;     ...
;                 const int row = row0 + ai * HALF + m * 16, pos = row & (MS - 1);
;                 const float rs = rstd[row];
; #pragma unroll
;                 for (int bj = 0; bj < 2; ++bj) {
;                     const int c0 = u.pn * BM + bj * HALF + wc * 32 + 8 * fq;
;                     f32x4 v0 = acc[ai][bj][m][0] * rs, v1 = acc[ai][bj][m][1] * rs;
;                     if (kind <= 1) {
;                         float s = (v0[0] * v0[0] + v0[1] * v0[1]) + (v0[2] * v0[2] + v0[3] * v0[3]) + (v1[0] * v1[0] + v1[1] * v1[1]) + (v1[2] * v1[2] + v1[3] * v1[3]);
;                         s += __shfl_xor(s, 16); s += __shfl_xor(s, 32);
;                         const int head = (u.pn & 3) * 2 + bj;
;                         if (fq == 0) ssq[(size_t)((kind * 8 + head) * 4 + wc) * MT + row] = s;
;                     } else if (kind <= 3) {
;                         const int i0 = (c0 & 127) >> 1;
;                         const f32x4 csa = *(const f32x4*)(cs + (size_t)pos * 64 + i0), csb = *(const f32x4*)(cs + (size_t)pos * 64 + i0 + 2);
;                         const float sc = (kind == 3) ? KSCALE : 1.0f;
;                         f32x4 w0, w1;
;                         w0[0] = (v0[0] * csa[0] - v0[1] * csa[1]) * sc; w0[1] = (v0[1] * csa[0] + v0[0] * csa[1]) * sc;
;                         w0[2] = (v0[2] * csa[2] - v0[3] * csa[3]) * sc; w0[3] = (v0[3] * csa[2] + v0[2] * csa[3]) * sc;
;                         w1[0] = (v1[0] * csb[0] - v1[1] * csb[1]) * sc; w1[1] = (v1[1] * csb[0] + v1[0] * csb[1]) * sc;
;                         w1[2] = (v1[2] * csb[2] - v1[3] * csb[3]) * sc; w1[3] = (v1[3] * csb[2] + v1[2] * csb[3]) * sc;
;                         v0 = w0; v1 = w1;
.LBB0_229:
	s_andn2_b64 vcc, exec, s[2:3]
	s_cbranch_vccnz .LBB0_231
	v_lshlrev_b32_e32 v184, 3, v163
	v_lshl_add_u64 v[150:151], v[136:137], 0, v[184:185]
	v_mov_b32_e32 v236, v150
	v_mov_b32_e32 v237, v151
	global_load_dwordx4 v[168:171], v[236:237], off
	global_load_dwordx4 v[172:175], v[236:237], off offset:16
	s_mov_b32 s100, 0x2000
	s_mov_b32 s101, 0
	v_lshl_add_u64 v[234:235], v[236:237], 0, s[100:101]
	global_load_dwordx4 v[176:179], v[234:235], off
	global_load_dwordx4 v[180:183], v[234:235], off offset:16
	s_mov_b32 s100, 0x4000
	s_mov_b32 s101, 0
	v_lshl_add_u64 v[234:235], v[236:237], 0, s[100:101]
	global_load_dwordx4 v[194:197], v[234:235], off
	global_load_dwordx4 v[198:201], v[234:235], off offset:16
	s_mov_b32 s100, 0x6000
	s_mov_b32 s101, 0
	v_lshl_add_u64 v[234:235], v[236:237], 0, s[100:101]
	global_load_dwordx4 v[202:205], v[234:235], off
	global_load_dwordx4 v[206:209], v[234:235], off offset:16
	s_waitcnt vmcnt(6)
	v_mov_b32_e32 v154, v172
	v_mov_b32_e32 v155, v173
	v_mov_b32_e32 v156, v174
	v_mov_b32_e32 v157, v175
	v_mov_b32_e32 v150, v168
	v_mov_b32_e32 v151, v169
	v_mov_b32_e32 v152, v170
	v_mov_b32_e32 v153, v171
	v_pk_mul_f32 v[164:165], v[124:125], v[150:151] op_sel:[1,1] op_sel_hi:[0,1]
	v_pk_fma_f32 v[166:167], v[124:125], v[150:151], v[164:165] neg_lo:[0,0,1] neg_hi:[0,0,1]
	v_pk_fma_f32 v[150:151], v[124:125], v[150:151], v[164:165] op_sel_hi:[1,0,1]
	v_mul_f32_e32 v164, v127, v153
	v_mov_b32_e32 v167, v151
	v_pk_mul_f32 v[150:151], v[144:145], v[166:167] op_sel_hi:[0,1]
	v_mul_f32_e32 v166, v127, v152
	v_pk_fma_f32 v[164:165], v[126:127], v[152:153], v[164:165] op_sel_hi:[1,1,0] neg_lo:[0,0,1] neg_hi:[0,0,1]
	v_pk_fma_f32 v[152:153], v[126:127], v[152:153], v[166:167] op_sel:[1,0,0] op_sel_hi:[0,1,0]
	v_mov_b32_e32 v165, v153
	v_pk_mul_f32 v[152:153], v[144:145], v[164:165] op_sel_hi:[0,1]
	v_pk_mul_f32 v[164:165], v[120:121], v[154:155] op_sel:[1,1] op_sel_hi:[0,1]
	v_pk_fma_f32 v[166:167], v[120:121], v[154:155], v[164:165] neg_lo:[0,0,1] neg_hi:[0,0,1]
	v_pk_fma_f32 v[154:155], v[120:121], v[154:155], v[164:165] op_sel_hi:[1,0,1]
	v_mul_f32_e32 v164, v123, v157
	v_mov_b32_e32 v167, v155
	v_pk_mul_f32 v[154:155], v[144:145], v[166:167] op_sel_hi:[0,1]
	v_mul_f32_e32 v166, v123, v156
	v_pk_fma_f32 v[164:165], v[122:123], v[156:157], v[164:165] op_sel_hi:[1,1,0] neg_lo:[0,0,1] neg_hi:[0,0,1]
	v_pk_fma_f32 v[156:157], v[122:123], v[156:157], v[166:167] op_sel:[1,0,0] op_sel_hi:[0,1,0]
	v_mov_b32_e32 v165, v157
	v_pk_mul_f32 v[156:157], v[144:145], v[164:165] op_sel_hi:[0,1]

;     __device__ __forceinline__ void operator()(const f32x4 (&acc)[2][2][4][2], const Unit& u, int wr, int wc, int fr, int fq) const {
;     ...
;                     const int c0 = u.pn * BM + bj * HALF + wc * 32 + 8 * fq;
;                     f32x4 v0 = acc[ai][bj][m][0] * rs, v1 = acc[ai][bj][m][1] * rs;
;                     if (kind <= 1) {
;                         float s = (v0[0] * v0[0] + v0[1] * v0[1]) + (v0[2] * v0[2] + v0[3] * v0[3]) + (v1[0] * v1[0] + v1[1] * v1[1]) + (v1[2] * v1[2] + v1[3] * v1[3]);
;                         s += __shfl_xor(s, 16); s += __shfl_xor(s, 32);
;                         const int head = (u.pn & 3) * 2 + bj;
;                         if (fq == 0) ssq[(size_t)((kind * 8 + head) * 4 + wc) * MT + row] = s;
;                     } else if (kind <= 3) {
;                         const int i0 = (c0 & 127) >> 1;
;                         const f32x4 csa = *(const f32x4*)(cs + (size_t)pos * 64 + i0), csb = *(const f32x4*)(cs + (size_t)pos * 64 + i0 + 2);
;                         const float sc = (kind == 3) ? KSCALE : 1.0f;
;                         f32x4 w0, w1;
;                         w0[0] = (v0[0] * csa[0] - v0[1] * csa[1]) * sc; w0[1] = (v0[1] * csa[0] + v0[0] * csa[1]) * sc;
;                         w0[2] = (v0[2] * csa[2] - v0[3] * csa[3]) * sc; w0[3] = (v0[3] * csa[2] + v0[2] * csa[3]) * sc;
;                         w1[0] = (v1[0] * csb[0] - v1[1] * csb[1]) * sc; w1[1] = (v1[1] * csb[0] + v1[0] * csb[1]) * sc;
;                         w1[2] = (v1[2] * csb[2] - v1[3] * csb[3]) * sc; w1[3] = (v1[3] * csb[2] + v1[2] * csb[3]) * sc;
;                         v0 = w0; v1 = w1;
.LBB0_239:
	s_andn2_b64 vcc, exec, s[0:1]
	s_cbranch_vccnz .LBB0_241
	v_lshlrev_b32_e32 v184, 3, v163
	v_lshl_add_u64 v[124:125], v[136:137], 0, v[184:185]
	v_mov_b32_e32 v148, v172
	v_mov_b32_e32 v149, v173
	v_mov_b32_e32 v150, v174
	v_mov_b32_e32 v151, v175
	v_mov_b32_e32 v124, v168
	v_mov_b32_e32 v125, v169
	v_mov_b32_e32 v126, v170
	v_mov_b32_e32 v127, v171
	v_pk_mul_f32 v[152:153], v[116:117], v[124:125] op_sel:[1,1] op_sel_hi:[0,1]
	v_pk_fma_f32 v[154:155], v[116:117], v[124:125], v[152:153] neg_lo:[0,0,1] neg_hi:[0,0,1]
	v_pk_fma_f32 v[124:125], v[116:117], v[124:125], v[152:153] op_sel_hi:[1,0,1]
	v_mul_f32_e32 v152, v119, v127
	v_mov_b32_e32 v155, v125
	v_pk_mul_f32 v[124:125], v[144:145], v[154:155] op_sel_hi:[0,1]
	v_mul_f32_e32 v154, v119, v126
	v_pk_fma_f32 v[152:153], v[118:119], v[126:127], v[152:153] op_sel_hi:[1,1,0] neg_lo:[0,0,1] neg_hi:[0,0,1]
	v_pk_fma_f32 v[126:127], v[118:119], v[126:127], v[154:155] op_sel:[1,0,0] op_sel_hi:[0,1,0]
	v_mov_b32_e32 v153, v127
	v_pk_mul_f32 v[126:127], v[144:145], v[152:153] op_sel_hi:[0,1]
	v_pk_mul_f32 v[152:153], v[112:113], v[148:149] op_sel:[1,1] op_sel_hi:[0,1]
	v_pk_fma_f32 v[154:155], v[112:113], v[148:149], v[152:153] neg_lo:[0,0,1] neg_hi:[0,0,1]
	v_pk_fma_f32 v[148:149], v[112:113], v[148:149], v[152:153] op_sel_hi:[1,0,1]
	v_mul_f32_e32 v152, v115, v151
	v_mov_b32_e32 v155, v149
	v_pk_mul_f32 v[148:149], v[144:145], v[154:155] op_sel_hi:[0,1]
	v_mul_f32_e32 v154, v115, v150
	v_pk_fma_f32 v[152:153], v[114:115], v[150:151], v[152:153] op_sel_hi:[1,1,0] neg_lo:[0,0,1] neg_hi:[0,0,1]
	v_pk_fma_f32 v[150:151], v[114:115], v[150:151], v[154:155] op_sel:[1,0,0] op_sel_hi:[0,1,0]
	v_mov_b32_e32 v153, v151
	v_pk_mul_f32 v[150:151], v[144:145], v[152:153] op_sel_hi:[0,1]

;     __device__ __forceinline__ void operator()(const f32x4 (&acc)[2][2][4][2], const Unit& u, int wr, int wc, int fr, int fq) const {
;     ...
;                     const int c0 = u.pn * BM + bj * HALF + wc * 32 + 8 * fq;
;                     f32x4 v0 = acc[ai][bj][m][0] * rs, v1 = acc[ai][bj][m][1] * rs;
;                     if (kind <= 1) {
;                         float s = (v0[0] * v0[0] + v0[1] * v0[1]) + (v0[2] * v0[2] + v0[3] * v0[3]) + (v1[0] * v1[0] + v1[1] * v1[1]) + (v1[2] * v1[2] + v1[3] * v1[3]);
;                         s += __shfl_xor(s, 16); s += __shfl_xor(s, 32);
;                         const int head = (u.pn & 3) * 2 + bj;
;                         if (fq == 0) ssq[(size_t)((kind * 8 + head) * 4 + wc) * MT + row] = s;
;                     } else if (kind <= 3) {
;                         const int i0 = (c0 & 127) >> 1;
;                         const f32x4 csa = *(const f32x4*)(cs + (size_t)pos * 64 + i0), csb = *(const f32x4*)(cs + (size_t)pos * 64 + i0 + 2);
;                         const float sc = (kind == 3) ? KSCALE : 1.0f;
;                         f32x4 w0, w1;
;                         w0[0] = (v0[0] * csa[0] - v0[1] * csa[1]) * sc; w0[1] = (v0[1] * csa[0] + v0[0] * csa[1]) * sc;
;                         w0[2] = (v0[2] * csa[2] - v0[3] * csa[3]) * sc; w0[3] = (v0[3] * csa[2] + v0[2] * csa[3]) * sc;
;                         w1[0] = (v1[0] * csb[0] - v1[1] * csb[1]) * sc; w1[1] = (v1[1] * csb[0] + v1[0] * csb[1]) * sc;
;                         w1[2] = (v1[2] * csb[2] - v1[3] * csb[3]) * sc; w1[3] = (v1[3] * csb[2] + v1[2] * csb[3]) * sc;
;                         v0 = w0; v1 = w1;
.LBB0_249:
	s_andn2_b64 vcc, exec, s[0:1]
	s_cbranch_vccnz .LBB0_251
	v_lshlrev_b32_e32 v184, 3, v115
	v_lshl_add_u64 v[116:117], v[136:137], 0, v[184:185]
	s_mov_b32 s100, 0x10000
	s_mov_b32 s101, 0
	v_lshl_add_u64 v[234:235], v[236:237], 0, s[100:101]
	global_load_dwordx4 v[168:171], v[234:235], off
	global_load_dwordx4 v[172:175], v[234:235], off offset:16
	s_waitcnt vmcnt(8)
	v_mov_b32_e32 v122, v180
	v_mov_b32_e32 v123, v181
	v_mov_b32_e32 v124, v182
	v_mov_b32_e32 v125, v183
	v_mov_b32_e32 v116, v176
	v_mov_b32_e32 v117, v177
	v_mov_b32_e32 v118, v178
	v_mov_b32_e32 v119, v179
	v_pk_mul_f32 v[126:127], v[108:109], v[116:117] op_sel:[1,1] op_sel_hi:[0,1]
	v_pk_fma_f32 v[148:149], v[108:109], v[116:117], v[126:127] neg_lo:[0,0,1] neg_hi:[0,0,1]
	v_pk_fma_f32 v[116:117], v[108:109], v[116:117], v[126:127] op_sel_hi:[1,0,1]
	v_mul_f32_e32 v126, v111, v119
	v_mov_b32_e32 v149, v117
	v_pk_mul_f32 v[116:117], v[144:145], v[148:149] op_sel_hi:[0,1]
	v_mul_f32_e32 v148, v111, v118
	v_pk_fma_f32 v[126:127], v[110:111], v[118:119], v[126:127] op_sel_hi:[1,1,0] neg_lo:[0,0,1] neg_hi:[0,0,1]
	v_pk_fma_f32 v[118:119], v[110:111], v[118:119], v[148:149] op_sel:[1,0,0] op_sel_hi:[0,1,0]
	v_mov_b32_e32 v127, v119
	v_pk_mul_f32 v[118:119], v[144:145], v[126:127] op_sel_hi:[0,1]
	v_pk_mul_f32 v[126:127], v[104:105], v[122:123] op_sel:[1,1] op_sel_hi:[0,1]
	v_pk_fma_f32 v[148:149], v[104:105], v[122:123], v[126:127] neg_lo:[0,0,1] neg_hi:[0,0,1]
	v_pk_fma_f32 v[122:123], v[104:105], v[122:123], v[126:127] op_sel_hi:[1,0,1]
	v_mul_f32_e32 v126, v107, v125
	v_mov_b32_e32 v149, v123
	v_pk_mul_f32 v[122:123], v[144:145], v[148:149] op_sel_hi:[0,1]
	v_mul_f32_e32 v148, v107, v124
	v_pk_fma_f32 v[126:127], v[106:107], v[124:125], v[126:127] op_sel_hi:[1,1,0] neg_lo:[0,0,1] neg_hi:[0,0,1]
	v_pk_fma_f32 v[124:125], v[106:107], v[124:125], v[148:149] op_sel:[1,0,0] op_sel_hi:[0,1,0]
	v_mov_b32_e32 v127, v125
	v_pk_mul_f32 v[124:125], v[144:145], v[126:127] op_sel_hi:[0,1]

;     __device__ __forceinline__ void operator()(const f32x4 (&acc)[2][2][4][2], const Unit& u, int wr, int wc, int fr, int fq) const {
;     ...
;                     const int c0 = u.pn * BM + bj * HALF + wc * 32 + 8 * fq;
;                     f32x4 v0 = acc[ai][bj][m][0] * rs, v1 = acc[ai][bj][m][1] * rs;
;                     if (kind <= 1) {
;                         float s = (v0[0] * v0[0] + v0[1] * v0[1]) + (v0[2] * v0[2] + v0[3] * v0[3]) + (v1[0] * v1[0] + v1[1] * v1[1]) + (v1[2] * v1[2] + v1[3] * v1[3]);
;                         s += __shfl_xor(s, 16); s += __shfl_xor(s, 32);
;                         const int head = (u.pn & 3) * 2 + bj;
;                         if (fq == 0) ssq[(size_t)((kind * 8 + head) * 4 + wc) * MT + row] = s;
;                     } else if (kind <= 3) {
;                         const int i0 = (c0 & 127) >> 1;
;                         const f32x4 csa = *(const f32x4*)(cs + (size_t)pos * 64 + i0), csb = *(const f32x4*)(cs + (size_t)pos * 64 + i0 + 2);
;                         const float sc = (kind == 3) ? KSCALE : 1.0f;
;                         f32x4 w0, w1;
;                         w0[0] = (v0[0] * csa[0] - v0[1] * csa[1]) * sc; w0[1] = (v0[1] * csa[0] + v0[0] * csa[1]) * sc;
;                         w0[2] = (v0[2] * csa[2] - v0[3] * csa[3]) * sc; w0[3] = (v0[3] * csa[2] + v0[2] * csa[3]) * sc;
;                         w1[0] = (v1[0] * csb[0] - v1[1] * csb[1]) * sc; w1[1] = (v1[1] * csb[0] + v1[0] * csb[1]) * sc;
;                         w1[2] = (v1[2] * csb[2] - v1[3] * csb[3]) * sc; w1[3] = (v1[3] * csb[2] + v1[2] * csb[3]) * sc;
;                         v0 = w0; v1 = w1;
.LBB0_259:
	s_andn2_b64 vcc, exec, s[0:1]
	s_cbranch_vccnz .LBB0_261
	v_lshlrev_b32_e32 v184, 3, v115
	v_lshl_add_u64 v[106:107], v[136:137], 0, v[184:185]
	v_mov_b32_e32 v110, v180
	v_mov_b32_e32 v111, v181
	v_mov_b32_e32 v112, v182
	v_mov_b32_e32 v113, v183
	v_mov_b32_e32 v106, v176
	v_mov_b32_e32 v107, v177
	v_mov_b32_e32 v108, v178
	v_mov_b32_e32 v109, v179
	v_pk_mul_f32 v[114:115], v[100:101], v[106:107] op_sel:[1,1] op_sel_hi:[0,1]
	v_pk_fma_f32 v[116:117], v[100:101], v[106:107], v[114:115] neg_lo:[0,0,1] neg_hi:[0,0,1]
	v_pk_fma_f32 v[106:107], v[100:101], v[106:107], v[114:115] op_sel_hi:[1,0,1]
	v_mul_f32_e32 v114, v103, v109
	v_mov_b32_e32 v117, v107
	v_pk_mul_f32 v[106:107], v[144:145], v[116:117] op_sel_hi:[0,1]
	v_mul_f32_e32 v116, v103, v108
	v_pk_fma_f32 v[114:115], v[102:103], v[108:109], v[114:115] op_sel_hi:[1,1,0] neg_lo:[0,0,1] neg_hi:[0,0,1]
	v_pk_fma_f32 v[108:109], v[102:103], v[108:109], v[116:117] op_sel:[1,0,0] op_sel_hi:[0,1,0]
	v_mov_b32_e32 v115, v109
	v_pk_mul_f32 v[108:109], v[144:145], v[114:115] op_sel_hi:[0,1]
	v_pk_mul_f32 v[114:115], v[96:97], v[110:111] op_sel:[1,1] op_sel_hi:[0,1]
	v_pk_fma_f32 v[116:117], v[96:97], v[110:111], v[114:115] neg_lo:[0,0,1] neg_hi:[0,0,1]
	v_pk_fma_f32 v[110:111], v[96:97], v[110:111], v[114:115] op_sel_hi:[1,0,1]
	v_mul_f32_e32 v114, v99, v113
	v_mov_b32_e32 v117, v111
	v_pk_mul_f32 v[110:111], v[144:145], v[116:117] op_sel_hi:[0,1]
	v_mul_f32_e32 v116, v99, v112
	v_pk_fma_f32 v[114:115], v[98:99], v[112:113], v[114:115] op_sel_hi:[1,1,0] neg_lo:[0,0,1] neg_hi:[0,0,1]
	v_pk_fma_f32 v[112:113], v[98:99], v[112:113], v[116:117] op_sel:[1,0,0] op_sel_hi:[0,1,0]
	v_mov_b32_e32 v115, v113
	v_pk_mul_f32 v[112:113], v[144:145], v[114:115] op_sel_hi:[0,1]

;     __device__ __forceinline__ void operator()(const f32x4 (&acc)[2][2][4][2], const Unit& u, int wr, int wc, int fr, int fq) const {
;     ...
;                     const int c0 = u.pn * BM + bj * HALF + wc * 32 + 8 * fq;
;                     f32x4 v0 = acc[ai][bj][m][0] * rs, v1 = acc[ai][bj][m][1] * rs;
;                     if (kind <= 1) {
;                         float s = (v0[0] * v0[0] + v0[1] * v0[1]) + (v0[2] * v0[2] + v0[3] * v0[3]) + (v1[0] * v1[0] + v1[1] * v1[1]) + (v1[2] * v1[2] + v1[3] * v1[3]);
;                         s += __shfl_xor(s, 16); s += __shfl_xor(s, 32);
;                         const int head = (u.pn & 3) * 2 + bj;
;                         if (fq == 0) ssq[(size_t)((kind * 8 + head) * 4 + wc) * MT + row] = s;
;                     } else if (kind <= 3) {
;                         const int i0 = (c0 & 127) >> 1;
;                         const f32x4 csa = *(const f32x4*)(cs + (size_t)pos * 64 + i0), csb = *(const f32x4*)(cs + (size_t)pos * 64 + i0 + 2);
;                         const float sc = (kind == 3) ? KSCALE : 1.0f;
;                         f32x4 w0, w1;
;                         w0[0] = (v0[0] * csa[0] - v0[1] * csa[1]) * sc; w0[1] = (v0[1] * csa[0] + v0[0] * csa[1]) * sc;
;                         w0[2] = (v0[2] * csa[2] - v0[3] * csa[3]) * sc; w0[3] = (v0[3] * csa[2] + v0[2] * csa[3]) * sc;
;                         w1[0] = (v1[0] * csb[0] - v1[1] * csb[1]) * sc; w1[1] = (v1[1] * csb[0] + v1[0] * csb[1]) * sc;
;                         w1[2] = (v1[2] * csb[2] - v1[3] * csb[3]) * sc; w1[3] = (v1[3] * csb[2] + v1[2] * csb[3]) * sc;
;                         v0 = w0; v1 = w1;
.LBB0_269:
	s_andn2_b64 vcc, exec, s[0:1]
	s_cbranch_vccnz .LBB0_271
	v_lshlrev_b32_e32 v184, 3, v99
	v_lshl_add_u64 v[100:101], v[136:137], 0, v[184:185]
	s_mov_b32 s100, 0x12000
	s_mov_b32 s101, 0
	v_lshl_add_u64 v[234:235], v[236:237], 0, s[100:101]
	global_load_dwordx4 v[176:179], v[234:235], off
	global_load_dwordx4 v[180:183], v[234:235], off offset:16
	s_waitcnt vmcnt(10)
	v_mov_b32_e32 v104, v198
	v_mov_b32_e32 v105, v199
	v_mov_b32_e32 v106, v200
	v_mov_b32_e32 v107, v201
	v_mov_b32_e32 v100, v194
	v_mov_b32_e32 v101, v195
	v_mov_b32_e32 v102, v196
	v_mov_b32_e32 v103, v197
	v_pk_mul_f32 v[108:109], v[92:93], v[100:101] op_sel:[1,1] op_sel_hi:[0,1]
	v_pk_fma_f32 v[110:111], v[92:93], v[100:101], v[108:109] neg_lo:[0,0,1] neg_hi:[0,0,1]
	v_pk_fma_f32 v[100:101], v[92:93], v[100:101], v[108:109] op_sel_hi:[1,0,1]
	v_mul_f32_e32 v108, v95, v103
	v_mov_b32_e32 v111, v101
	v_pk_mul_f32 v[100:101], v[144:145], v[110:111] op_sel_hi:[0,1]
	v_mul_f32_e32 v110, v95, v102
	v_pk_fma_f32 v[108:109], v[94:95], v[102:103], v[108:109] op_sel_hi:[1,1,0] neg_lo:[0,0,1] neg_hi:[0,0,1]
	v_pk_fma_f32 v[102:103], v[94:95], v[102:103], v[110:111] op_sel:[1,0,0] op_sel_hi:[0,1,0]
	v_mov_b32_e32 v109, v103
	v_pk_mul_f32 v[102:103], v[144:145], v[108:109] op_sel_hi:[0,1]
	v_pk_mul_f32 v[108:109], v[88:89], v[104:105] op_sel:[1,1] op_sel_hi:[0,1]
	v_pk_fma_f32 v[110:111], v[88:89], v[104:105], v[108:109] neg_lo:[0,0,1] neg_hi:[0,0,1]
	v_pk_fma_f32 v[104:105], v[88:89], v[104:105], v[108:109] op_sel_hi:[1,0,1]
	v_mul_f32_e32 v108, v91, v107
	v_mov_b32_e32 v111, v105
	v_pk_mul_f32 v[104:105], v[144:145], v[110:111] op_sel_hi:[0,1]
	v_mul_f32_e32 v110, v91, v106
	v_pk_fma_f32 v[108:109], v[90:91], v[106:107], v[108:109] op_sel_hi:[1,1,0] neg_lo:[0,0,1] neg_hi:[0,0,1]
	v_pk_fma_f32 v[106:107], v[90:91], v[106:107], v[110:111] op_sel:[1,0,0] op_sel_hi:[0,1,0]
	v_mov_b32_e32 v109, v107
	v_pk_mul_f32 v[106:107], v[144:145], v[108:109] op_sel_hi:[0,1]

;     __device__ __forceinline__ void operator()(const f32x4 (&acc)[2][2][4][2], const Unit& u, int wr, int wc, int fr, int fq) const {
;     ...
;                     const int c0 = u.pn * BM + bj * HALF + wc * 32 + 8 * fq;
;                     f32x4 v0 = acc[ai][bj][m][0] * rs, v1 = acc[ai][bj][m][1] * rs;
;                     if (kind <= 1) {
;                         float s = (v0[0] * v0[0] + v0[1] * v0[1]) + (v0[2] * v0[2] + v0[3] * v0[3]) + (v1[0] * v1[0] + v1[1] * v1[1]) + (v1[2] * v1[2] + v1[3] * v1[3]);
;                         s += __shfl_xor(s, 16); s += __shfl_xor(s, 32);
;                         const int head = (u.pn & 3) * 2 + bj;
;                         if (fq == 0) ssq[(size_t)((kind * 8 + head) * 4 + wc) * MT + row] = s;
;                     } else if (kind <= 3) {
;                         const int i0 = (c0 & 127) >> 1;
;                         const f32x4 csa = *(const f32x4*)(cs + (size_t)pos * 64 + i0), csb = *(const f32x4*)(cs + (size_t)pos * 64 + i0 + 2);
;                         const float sc = (kind == 3) ? KSCALE : 1.0f;
;                         f32x4 w0, w1;
;                         w0[0] = (v0[0] * csa[0] - v0[1] * csa[1]) * sc; w0[1] = (v0[1] * csa[0] + v0[0] * csa[1]) * sc;
;                         w0[2] = (v0[2] * csa[2] - v0[3] * csa[3]) * sc; w0[3] = (v0[3] * csa[2] + v0[2] * csa[3]) * sc;
;                         w1[0] = (v1[0] * csb[0] - v1[1] * csb[1]) * sc; w1[1] = (v1[1] * csb[0] + v1[0] * csb[1]) * sc;
;                         w1[2] = (v1[2] * csb[2] - v1[3] * csb[3]) * sc; w1[3] = (v1[3] * csb[2] + v1[2] * csb[3]) * sc;
;                         v0 = w0; v1 = w1;
.LBB0_279:
	s_andn2_b64 vcc, exec, s[0:1]
	s_cbranch_vccnz .LBB0_281
	v_lshlrev_b32_e32 v184, 3, v99
	v_lshl_add_u64 v[90:91], v[136:137], 0, v[184:185]
	v_mov_b32_e32 v94, v198
	v_mov_b32_e32 v95, v199
	v_mov_b32_e32 v96, v200
	v_mov_b32_e32 v97, v201
	v_mov_b32_e32 v90, v194
	v_mov_b32_e32 v91, v195
	v_mov_b32_e32 v92, v196
	v_mov_b32_e32 v93, v197
	v_pk_mul_f32 v[98:99], v[84:85], v[90:91] op_sel:[1,1] op_sel_hi:[0,1]
	v_pk_fma_f32 v[100:101], v[84:85], v[90:91], v[98:99] neg_lo:[0,0,1] neg_hi:[0,0,1]
	v_pk_fma_f32 v[90:91], v[84:85], v[90:91], v[98:99] op_sel_hi:[1,0,1]
	v_mul_f32_e32 v98, v87, v93
	v_mov_b32_e32 v101, v91
	v_pk_mul_f32 v[90:91], v[144:145], v[100:101] op_sel_hi:[0,1]
	v_mul_f32_e32 v100, v87, v92
	v_pk_fma_f32 v[98:99], v[86:87], v[92:93], v[98:99] op_sel_hi:[1,1,0] neg_lo:[0,0,1] neg_hi:[0,0,1]
	v_pk_fma_f32 v[92:93], v[86:87], v[92:93], v[100:101] op_sel:[1,0,0] op_sel_hi:[0,1,0]
	v_mov_b32_e32 v99, v93
	v_pk_mul_f32 v[92:93], v[144:145], v[98:99] op_sel_hi:[0,1]
	v_pk_mul_f32 v[98:99], v[80:81], v[94:95] op_sel:[1,1] op_sel_hi:[0,1]
	v_pk_fma_f32 v[100:101], v[80:81], v[94:95], v[98:99] neg_lo:[0,0,1] neg_hi:[0,0,1]
	v_pk_fma_f32 v[94:95], v[80:81], v[94:95], v[98:99] op_sel_hi:[1,0,1]
	v_mul_f32_e32 v98, v83, v97
	v_mov_b32_e32 v101, v95
	v_pk_mul_f32 v[94:95], v[144:145], v[100:101] op_sel_hi:[0,1]
	v_mul_f32_e32 v100, v83, v96
	v_pk_fma_f32 v[98:99], v[82:83], v[96:97], v[98:99] op_sel_hi:[1,1,0] neg_lo:[0,0,1] neg_hi:[0,0,1]
	v_pk_fma_f32 v[96:97], v[82:83], v[96:97], v[100:101] op_sel:[1,0,0] op_sel_hi:[0,1,0]
	v_mov_b32_e32 v99, v97
	v_pk_mul_f32 v[96:97], v[144:145], v[98:99] op_sel_hi:[0,1]

;     __device__ __forceinline__ void operator()(const f32x4 (&acc)[2][2][4][2], const Unit& u, int wr, int wc, int fr, int fq) const {
;     ...
;                     const int c0 = u.pn * BM + bj * HALF + wc * 32 + 8 * fq;
;                     f32x4 v0 = acc[ai][bj][m][0] * rs, v1 = acc[ai][bj][m][1] * rs;
;                     if (kind <= 1) {
;                         float s = (v0[0] * v0[0] + v0[1] * v0[1]) + (v0[2] * v0[2] + v0[3] * v0[3]) + (v1[0] * v1[0] + v1[1] * v1[1]) + (v1[2] * v1[2] + v1[3] * v1[3]);
;                         s += __shfl_xor(s, 16); s += __shfl_xor(s, 32);
;                         const int head = (u.pn & 3) * 2 + bj;
;                         if (fq == 0) ssq[(size_t)((kind * 8 + head) * 4 + wc) * MT + row] = s;
;                     } else if (kind <= 3) {
;                         const int i0 = (c0 & 127) >> 1;
;                         const f32x4 csa = *(const f32x4*)(cs + (size_t)pos * 64 + i0), csb = *(const f32x4*)(cs + (size_t)pos * 64 + i0 + 2);
;                         const float sc = (kind == 3) ? KSCALE : 1.0f;
;                         f32x4 w0, w1;
;                         w0[0] = (v0[0] * csa[0] - v0[1] * csa[1]) * sc; w0[1] = (v0[1] * csa[0] + v0[0] * csa[1]) * sc;
;                         w0[2] = (v0[2] * csa[2] - v0[3] * csa[3]) * sc; w0[3] = (v0[3] * csa[2] + v0[2] * csa[3]) * sc;
;                         w1[0] = (v1[0] * csb[0] - v1[1] * csb[1]) * sc; w1[1] = (v1[1] * csb[0] + v1[0] * csb[1]) * sc;
;                         w1[2] = (v1[2] * csb[2] - v1[3] * csb[3]) * sc; w1[3] = (v1[3] * csb[2] + v1[2] * csb[3]) * sc;
;                         v0 = w0; v1 = w1;
.LBB0_289:
	s_andn2_b64 vcc, exec, s[0:1]
	s_cbranch_vccnz .LBB0_291
	v_lshlrev_b32_e32 v184, 3, v83
	v_lshl_add_u64 v[84:85], v[136:137], 0, v[184:185]
	s_mov_b32 s100, 0x14000
	s_mov_b32 s101, 0
	v_lshl_add_u64 v[234:235], v[236:237], 0, s[100:101]
	global_load_dwordx4 v[194:197], v[234:235], off
	global_load_dwordx4 v[198:201], v[234:235], off offset:16
	s_waitcnt vmcnt(12)
	v_mov_b32_e32 v88, v206
	v_mov_b32_e32 v89, v207
	v_mov_b32_e32 v90, v208
	v_mov_b32_e32 v91, v209
	v_mov_b32_e32 v84, v202
	v_mov_b32_e32 v85, v203
	v_mov_b32_e32 v86, v204
	v_mov_b32_e32 v87, v205
	v_pk_mul_f32 v[92:93], v[76:77], v[84:85] op_sel:[1,1] op_sel_hi:[0,1]
	v_pk_fma_f32 v[94:95], v[76:77], v[84:85], v[92:93] neg_lo:[0,0,1] neg_hi:[0,0,1]
	v_pk_fma_f32 v[84:85], v[76:77], v[84:85], v[92:93] op_sel_hi:[1,0,1]
	v_mul_f32_e32 v92, v79, v87
	v_mov_b32_e32 v95, v85
	v_pk_mul_f32 v[84:85], v[144:145], v[94:95] op_sel_hi:[0,1]
	v_mul_f32_e32 v94, v79, v86
	v_pk_fma_f32 v[92:93], v[78:79], v[86:87], v[92:93] op_sel_hi:[1,1,0] neg_lo:[0,0,1] neg_hi:[0,0,1]
	v_pk_fma_f32 v[86:87], v[78:79], v[86:87], v[94:95] op_sel:[1,0,0] op_sel_hi:[0,1,0]
	v_mov_b32_e32 v93, v87
	v_pk_mul_f32 v[86:87], v[144:145], v[92:93] op_sel_hi:[0,1]
	v_pk_mul_f32 v[92:93], v[72:73], v[88:89] op_sel:[1,1] op_sel_hi:[0,1]
	v_pk_fma_f32 v[94:95], v[72:73], v[88:89], v[92:93] neg_lo:[0,0,1] neg_hi:[0,0,1]
	v_pk_fma_f32 v[88:89], v[72:73], v[88:89], v[92:93] op_sel_hi:[1,0,1]
	v_mul_f32_e32 v92, v75, v91
	v_mov_b32_e32 v95, v89
	v_pk_mul_f32 v[88:89], v[144:145], v[94:95] op_sel_hi:[0,1]
	v_mul_f32_e32 v94, v75, v90
	v_pk_fma_f32 v[92:93], v[74:75], v[90:91], v[92:93] op_sel_hi:[1,1,0] neg_lo:[0,0,1] neg_hi:[0,0,1]
	v_pk_fma_f32 v[90:91], v[74:75], v[90:91], v[94:95] op_sel:[1,0,0] op_sel_hi:[0,1,0]
	v_mov_b32_e32 v93, v91
	v_pk_mul_f32 v[90:91], v[144:145], v[92:93] op_sel_hi:[0,1]

;     __device__ __forceinline__ void operator()(const f32x4 (&acc)[2][2][4][2], const Unit& u, int wr, int wc, int fr, int fq) const {
;     ...
;                     const int c0 = u.pn * BM + bj * HALF + wc * 32 + 8 * fq;
;                     f32x4 v0 = acc[ai][bj][m][0] * rs, v1 = acc[ai][bj][m][1] * rs;
;                     if (kind <= 1) {
;                         float s = (v0[0] * v0[0] + v0[1] * v0[1]) + (v0[2] * v0[2] + v0[3] * v0[3]) + (v1[0] * v1[0] + v1[1] * v1[1]) + (v1[2] * v1[2] + v1[3] * v1[3]);
;                         s += __shfl_xor(s, 16); s += __shfl_xor(s, 32);
;                         const int head = (u.pn & 3) * 2 + bj;
;                         if (fq == 0) ssq[(size_t)((kind * 8 + head) * 4 + wc) * MT + row] = s;
;                     } else if (kind <= 3) {
;                         const int i0 = (c0 & 127) >> 1;
;                         const f32x4 csa = *(const f32x4*)(cs + (size_t)pos * 64 + i0), csb = *(const f32x4*)(cs + (size_t)pos * 64 + i0 + 2);
;                         const float sc = (kind == 3) ? KSCALE : 1.0f;
;                         f32x4 w0, w1;
;                         w0[0] = (v0[0] * csa[0] - v0[1] * csa[1]) * sc; w0[1] = (v0[1] * csa[0] + v0[0] * csa[1]) * sc;
;                         w0[2] = (v0[2] * csa[2] - v0[3] * csa[3]) * sc; w0[3] = (v0[3] * csa[2] + v0[2] * csa[3]) * sc;
;                         w1[0] = (v1[0] * csb[0] - v1[1] * csb[1]) * sc; w1[1] = (v1[1] * csb[0] + v1[0] * csb[1]) * sc;
;                         w1[2] = (v1[2] * csb[2] - v1[3] * csb[3]) * sc; w1[3] = (v1[3] * csb[2] + v1[2] * csb[3]) * sc;
;                         v0 = w0; v1 = w1;
.LBB0_299:
	s_andn2_b64 vcc, exec, s[0:1]
	s_cbranch_vccnz .LBB0_301
	v_lshlrev_b32_e32 v184, 3, v83
	v_lshl_add_u64 v[74:75], v[136:137], 0, v[184:185]
	v_mov_b32_e32 v78, v206
	v_mov_b32_e32 v79, v207
	v_mov_b32_e32 v80, v208
	v_mov_b32_e32 v81, v209
	v_mov_b32_e32 v74, v202
	v_mov_b32_e32 v75, v203
	v_mov_b32_e32 v76, v204
	v_mov_b32_e32 v77, v205
	v_pk_mul_f32 v[82:83], v[68:69], v[74:75] op_sel:[1,1] op_sel_hi:[0,1]
	v_pk_fma_f32 v[84:85], v[68:69], v[74:75], v[82:83] neg_lo:[0,0,1] neg_hi:[0,0,1]
	v_pk_fma_f32 v[74:75], v[68:69], v[74:75], v[82:83] op_sel_hi:[1,0,1]
	v_mul_f32_e32 v82, v71, v77
	v_mov_b32_e32 v85, v75
	v_pk_mul_f32 v[74:75], v[144:145], v[84:85] op_sel_hi:[0,1]
	v_mul_f32_e32 v84, v71, v76
	v_pk_fma_f32 v[82:83], v[70:71], v[76:77], v[82:83] op_sel_hi:[1,1,0] neg_lo:[0,0,1] neg_hi:[0,0,1]
	v_pk_fma_f32 v[76:77], v[70:71], v[76:77], v[84:85] op_sel:[1,0,0] op_sel_hi:[0,1,0]
	v_mov_b32_e32 v83, v77
	v_pk_mul_f32 v[76:77], v[144:145], v[82:83] op_sel_hi:[0,1]
	v_pk_mul_f32 v[82:83], v[64:65], v[78:79] op_sel:[1,1] op_sel_hi:[0,1]
	v_pk_fma_f32 v[84:85], v[64:65], v[78:79], v[82:83] neg_lo:[0,0,1] neg_hi:[0,0,1]
	v_pk_fma_f32 v[78:79], v[64:65], v[78:79], v[82:83] op_sel_hi:[1,0,1]
	v_mul_f32_e32 v82, v67, v81
	v_mov_b32_e32 v85, v79
	v_pk_mul_f32 v[78:79], v[144:145], v[84:85] op_sel_hi:[0,1]
	v_mul_f32_e32 v84, v67, v80
	v_pk_fma_f32 v[82:83], v[66:67], v[80:81], v[82:83] op_sel_hi:[1,1,0] neg_lo:[0,0,1] neg_hi:[0,0,1]
	v_pk_fma_f32 v[80:81], v[66:67], v[80:81], v[84:85] op_sel:[1,0,0] op_sel_hi:[0,1,0]
	v_mov_b32_e32 v83, v81
	v_pk_mul_f32 v[80:81], v[144:145], v[82:83] op_sel_hi:[0,1]

;     __device__ __forceinline__ void operator()(const f32x4 (&acc)[2][2][4][2], const Unit& u, int wr, int wc, int fr, int fq) const {
;     ...
;                     const int c0 = u.pn * BM + bj * HALF + wc * 32 + 8 * fq;
;                     f32x4 v0 = acc[ai][bj][m][0] * rs, v1 = acc[ai][bj][m][1] * rs;
;                     if (kind <= 1) {
;                         float s = (v0[0] * v0[0] + v0[1] * v0[1]) + (v0[2] * v0[2] + v0[3] * v0[3]) + (v1[0] * v1[0] + v1[1] * v1[1]) + (v1[2] * v1[2] + v1[3] * v1[3]);
;                         s += __shfl_xor(s, 16); s += __shfl_xor(s, 32);
;                         const int head = (u.pn & 3) * 2 + bj;
;                         if (fq == 0) ssq[(size_t)((kind * 8 + head) * 4 + wc) * MT + row] = s;
;                     } else if (kind <= 3) {
;                         const int i0 = (c0 & 127) >> 1;
;                         const f32x4 csa = *(const f32x4*)(cs + (size_t)pos * 64 + i0), csb = *(const f32x4*)(cs + (size_t)pos * 64 + i0 + 2);
;                         const float sc = (kind == 3) ? KSCALE : 1.0f;
;                         f32x4 w0, w1;
;                         w0[0] = (v0[0] * csa[0] - v0[1] * csa[1]) * sc; w0[1] = (v0[1] * csa[0] + v0[0] * csa[1]) * sc;
;                         w0[2] = (v0[2] * csa[2] - v0[3] * csa[3]) * sc; w0[3] = (v0[3] * csa[2] + v0[2] * csa[3]) * sc;
;                         w1[0] = (v1[0] * csb[0] - v1[1] * csb[1]) * sc; w1[1] = (v1[1] * csb[0] + v1[0] * csb[1]) * sc;
;                         w1[2] = (v1[2] * csb[2] - v1[3] * csb[3]) * sc; w1[3] = (v1[3] * csb[2] + v1[2] * csb[3]) * sc;
;                         v0 = w0; v1 = w1;
.LBB0_309:
	s_andn2_b64 vcc, exec, s[0:1]
	s_cbranch_vccnz .LBB0_311
	v_lshlrev_b32_e32 v184, 3, v74
	v_lshl_add_u64 v[66:67], v[136:137], 0, v[184:185]
	s_mov_b32 s100, 0x16000
	s_mov_b32 s101, 0
	v_lshl_add_u64 v[234:235], v[236:237], 0, s[100:101]
	global_load_dwordx4 v[202:205], v[234:235], off
	global_load_dwordx4 v[206:209], v[234:235], off offset:16
	s_waitcnt vmcnt(12)
	v_mov_b32_e32 v70, v172
	v_mov_b32_e32 v71, v173
	v_mov_b32_e32 v72, v174
	v_mov_b32_e32 v73, v175
	v_mov_b32_e32 v66, v168
	v_mov_b32_e32 v67, v169
	v_mov_b32_e32 v68, v170
	v_mov_b32_e32 v69, v171
	v_pk_mul_f32 v[76:77], v[60:61], v[66:67] op_sel:[1,1] op_sel_hi:[0,1]
	v_pk_fma_f32 v[78:79], v[60:61], v[66:67], v[76:77] neg_lo:[0,0,1] neg_hi:[0,0,1]
	v_pk_fma_f32 v[66:67], v[60:61], v[66:67], v[76:77] op_sel_hi:[1,0,1]
	v_mul_f32_e32 v76, v63, v69
	v_mov_b32_e32 v79, v67
	v_pk_mul_f32 v[66:67], v[144:145], v[78:79] op_sel_hi:[0,1]
	v_mul_f32_e32 v78, v63, v68
	v_pk_fma_f32 v[76:77], v[62:63], v[68:69], v[76:77] op_sel_hi:[1,1,0] neg_lo:[0,0,1] neg_hi:[0,0,1]
	v_pk_fma_f32 v[68:69], v[62:63], v[68:69], v[78:79] op_sel:[1,0,0] op_sel_hi:[0,1,0]
	v_mov_b32_e32 v77, v69
	v_pk_mul_f32 v[68:69], v[144:145], v[76:77] op_sel_hi:[0,1]
	v_pk_mul_f32 v[76:77], v[56:57], v[70:71] op_sel:[1,1] op_sel_hi:[0,1]
	v_pk_fma_f32 v[78:79], v[56:57], v[70:71], v[76:77] neg_lo:[0,0,1] neg_hi:[0,0,1]
	v_pk_fma_f32 v[70:71], v[56:57], v[70:71], v[76:77] op_sel_hi:[1,0,1]
	v_mul_f32_e32 v76, v59, v73
	v_mov_b32_e32 v79, v71
	v_pk_mul_f32 v[70:71], v[144:145], v[78:79] op_sel_hi:[0,1]
	v_mul_f32_e32 v78, v59, v72
	v_pk_fma_f32 v[76:77], v[58:59], v[72:73], v[76:77] op_sel_hi:[1,1,0] neg_lo:[0,0,1] neg_hi:[0,0,1]
	v_pk_fma_f32 v[72:73], v[58:59], v[72:73], v[78:79] op_sel:[1,0,0] op_sel_hi:[0,1,0]
	v_mov_b32_e32 v77, v73
	v_pk_mul_f32 v[72:73], v[144:145], v[76:77] op_sel_hi:[0,1]

;     __device__ __forceinline__ void operator()(const f32x4 (&acc)[2][2][4][2], const Unit& u, int wr, int wc, int fr, int fq) const {
;     ...
;                     const int c0 = u.pn * BM + bj * HALF + wc * 32 + 8 * fq;
;                     f32x4 v0 = acc[ai][bj][m][0] * rs, v1 = acc[ai][bj][m][1] * rs;
;                     if (kind <= 1) {
;                         float s = (v0[0] * v0[0] + v0[1] * v0[1]) + (v0[2] * v0[2] + v0[3] * v0[3]) + (v1[0] * v1[0] + v1[1] * v1[1]) + (v1[2] * v1[2] + v1[3] * v1[3]);
;                         s += __shfl_xor(s, 16); s += __shfl_xor(s, 32);
;                         const int head = (u.pn & 3) * 2 + bj;
;                         if (fq == 0) ssq[(size_t)((kind * 8 + head) * 4 + wc) * MT + row] = s;
;                     } else if (kind <= 3) {
;                         const int i0 = (c0 & 127) >> 1;
;                         const f32x4 csa = *(const f32x4*)(cs + (size_t)pos * 64 + i0), csb = *(const f32x4*)(cs + (size_t)pos * 64 + i0 + 2);
;                         const float sc = (kind == 3) ? KSCALE : 1.0f;
;                         f32x4 w0, w1;
;                         w0[0] = (v0[0] * csa[0] - v0[1] * csa[1]) * sc; w0[1] = (v0[1] * csa[0] + v0[0] * csa[1]) * sc;
;                         w0[2] = (v0[2] * csa[2] - v0[3] * csa[3]) * sc; w0[3] = (v0[3] * csa[2] + v0[2] * csa[3]) * sc;
;                         w1[0] = (v1[0] * csb[0] - v1[1] * csb[1]) * sc; w1[1] = (v1[1] * csb[0] + v1[0] * csb[1]) * sc;
;                         w1[2] = (v1[2] * csb[2] - v1[3] * csb[3]) * sc; w1[3] = (v1[3] * csb[2] + v1[2] * csb[3]) * sc;
;                         v0 = w0; v1 = w1;
.LBB0_319:
	s_andn2_b64 vcc, exec, s[0:1]
	s_cbranch_vccnz .LBB0_321
	v_lshlrev_b32_e32 v184, 3, v74
	v_lshl_add_u64 v[58:59], v[136:137], 0, v[184:185]
	v_mov_b32_e32 v62, v172
	v_mov_b32_e32 v63, v173
	v_mov_b32_e32 v64, v174
	v_mov_b32_e32 v65, v175
	v_mov_b32_e32 v58, v168
	v_mov_b32_e32 v59, v169
	v_mov_b32_e32 v60, v170
	v_mov_b32_e32 v61, v171
	v_pk_mul_f32 v[66:67], v[52:53], v[58:59] op_sel:[1,1] op_sel_hi:[0,1]
	v_pk_fma_f32 v[68:69], v[52:53], v[58:59], v[66:67] neg_lo:[0,0,1] neg_hi:[0,0,1]
	v_pk_fma_f32 v[58:59], v[52:53], v[58:59], v[66:67] op_sel_hi:[1,0,1]
	v_mul_f32_e32 v66, v55, v61
	v_mov_b32_e32 v69, v59
	v_pk_mul_f32 v[58:59], v[144:145], v[68:69] op_sel_hi:[0,1]
	v_mul_f32_e32 v68, v55, v60
	v_pk_fma_f32 v[66:67], v[54:55], v[60:61], v[66:67] op_sel_hi:[1,1,0] neg_lo:[0,0,1] neg_hi:[0,0,1]
	v_pk_fma_f32 v[60:61], v[54:55], v[60:61], v[68:69] op_sel:[1,0,0] op_sel_hi:[0,1,0]
	v_mov_b32_e32 v67, v61
	v_pk_mul_f32 v[60:61], v[144:145], v[66:67] op_sel_hi:[0,1]
	v_pk_mul_f32 v[66:67], v[48:49], v[62:63] op_sel:[1,1] op_sel_hi:[0,1]
	v_pk_fma_f32 v[68:69], v[48:49], v[62:63], v[66:67] neg_lo:[0,0,1] neg_hi:[0,0,1]
	v_pk_fma_f32 v[62:63], v[48:49], v[62:63], v[66:67] op_sel_hi:[1,0,1]
	v_mul_f32_e32 v66, v51, v65
	v_mov_b32_e32 v69, v63
	v_pk_mul_f32 v[62:63], v[144:145], v[68:69] op_sel_hi:[0,1]
	v_mul_f32_e32 v68, v51, v64
	v_pk_fma_f32 v[66:67], v[50:51], v[64:65], v[66:67] op_sel_hi:[1,1,0] neg_lo:[0,0,1] neg_hi:[0,0,1]
	v_pk_fma_f32 v[64:65], v[50:51], v[64:65], v[68:69] op_sel:[1,0,0] op_sel_hi:[0,1,0]
	v_mov_b32_e32 v67, v65
	v_pk_mul_f32 v[64:65], v[144:145], v[66:67] op_sel_hi:[0,1]

;     __device__ __forceinline__ void operator()(const f32x4 (&acc)[2][2][4][2], const Unit& u, int wr, int wc, int fr, int fq) const {
;     ...
;                     const int c0 = u.pn * BM + bj * HALF + wc * 32 + 8 * fq;
;                     f32x4 v0 = acc[ai][bj][m][0] * rs, v1 = acc[ai][bj][m][1] * rs;
;                     if (kind <= 1) {
;                         float s = (v0[0] * v0[0] + v0[1] * v0[1]) + (v0[2] * v0[2] + v0[3] * v0[3]) + (v1[0] * v1[0] + v1[1] * v1[1]) + (v1[2] * v1[2] + v1[3] * v1[3]);
;                         s += __shfl_xor(s, 16); s += __shfl_xor(s, 32);
;                         const int head = (u.pn & 3) * 2 + bj;
;                         if (fq == 0) ssq[(size_t)((kind * 8 + head) * 4 + wc) * MT + row] = s;
;                     } else if (kind <= 3) {
;                         const int i0 = (c0 & 127) >> 1;
;                         const f32x4 csa = *(const f32x4*)(cs + (size_t)pos * 64 + i0), csb = *(const f32x4*)(cs + (size_t)pos * 64 + i0 + 2);
;                         const float sc = (kind == 3) ? KSCALE : 1.0f;
;                         f32x4 w0, w1;
;                         w0[0] = (v0[0] * csa[0] - v0[1] * csa[1]) * sc; w0[1] = (v0[1] * csa[0] + v0[0] * csa[1]) * sc;
;                         w0[2] = (v0[2] * csa[2] - v0[3] * csa[3]) * sc; w0[3] = (v0[3] * csa[2] + v0[2] * csa[3]) * sc;
;                         w1[0] = (v1[0] * csb[0] - v1[1] * csb[1]) * sc; w1[1] = (v1[1] * csb[0] + v1[0] * csb[1]) * sc;
;                         w1[2] = (v1[2] * csb[2] - v1[3] * csb[3]) * sc; w1[3] = (v1[3] * csb[2] + v1[2] * csb[3]) * sc;
;                         v0 = w0; v1 = w1;
.LBB0_329:
	s_andn2_b64 vcc, exec, s[0:1]
	s_cbranch_vccnz .LBB0_331
	v_lshlrev_b32_e32 v184, 3, v58
	v_lshl_add_u64 v[50:51], v[136:137], 0, v[184:185]
	s_waitcnt vmcnt(10)
	v_mov_b32_e32 v54, v180
	v_mov_b32_e32 v55, v181
	v_mov_b32_e32 v56, v182
	v_mov_b32_e32 v57, v183
	v_mov_b32_e32 v50, v176
	v_mov_b32_e32 v51, v177
	v_mov_b32_e32 v52, v178
	v_mov_b32_e32 v53, v179
	v_pk_mul_f32 v[60:61], v[44:45], v[50:51] op_sel:[1,1] op_sel_hi:[0,1]
	v_pk_fma_f32 v[62:63], v[44:45], v[50:51], v[60:61] neg_lo:[0,0,1] neg_hi:[0,0,1]
	v_pk_fma_f32 v[50:51], v[44:45], v[50:51], v[60:61] op_sel_hi:[1,0,1]
	v_mul_f32_e32 v60, v47, v53
	v_mov_b32_e32 v63, v51
	v_pk_mul_f32 v[50:51], v[144:145], v[62:63] op_sel_hi:[0,1]
	v_mul_f32_e32 v62, v47, v52
	v_pk_fma_f32 v[60:61], v[46:47], v[52:53], v[60:61] op_sel_hi:[1,1,0] neg_lo:[0,0,1] neg_hi:[0,0,1]
	v_pk_fma_f32 v[52:53], v[46:47], v[52:53], v[62:63] op_sel:[1,0,0] op_sel_hi:[0,1,0]
	v_mov_b32_e32 v61, v53
	v_pk_mul_f32 v[52:53], v[144:145], v[60:61] op_sel_hi:[0,1]
	v_pk_mul_f32 v[60:61], v[40:41], v[54:55] op_sel:[1,1] op_sel_hi:[0,1]
	v_pk_fma_f32 v[62:63], v[40:41], v[54:55], v[60:61] neg_lo:[0,0,1] neg_hi:[0,0,1]
	v_pk_fma_f32 v[54:55], v[40:41], v[54:55], v[60:61] op_sel_hi:[1,0,1]
	v_mul_f32_e32 v60, v43, v57
	v_mov_b32_e32 v63, v55
	v_pk_mul_f32 v[54:55], v[144:145], v[62:63] op_sel_hi:[0,1]
	v_mul_f32_e32 v62, v43, v56
	v_pk_fma_f32 v[60:61], v[42:43], v[56:57], v[60:61] op_sel_hi:[1,1,0] neg_lo:[0,0,1] neg_hi:[0,0,1]
	v_pk_fma_f32 v[56:57], v[42:43], v[56:57], v[62:63] op_sel:[1,0,0] op_sel_hi:[0,1,0]
	v_mov_b32_e32 v61, v57
	v_pk_mul_f32 v[56:57], v[144:145], v[60:61] op_sel_hi:[0,1]

;     __device__ __forceinline__ void operator()(const f32x4 (&acc)[2][2][4][2], const Unit& u, int wr, int wc, int fr, int fq) const {
;     ...
;                     const int c0 = u.pn * BM + bj * HALF + wc * 32 + 8 * fq;
;                     f32x4 v0 = acc[ai][bj][m][0] * rs, v1 = acc[ai][bj][m][1] * rs;
;                     if (kind <= 1) {
;                         float s = (v0[0] * v0[0] + v0[1] * v0[1]) + (v0[2] * v0[2] + v0[3] * v0[3]) + (v1[0] * v1[0] + v1[1] * v1[1]) + (v1[2] * v1[2] + v1[3] * v1[3]);
;                         s += __shfl_xor(s, 16); s += __shfl_xor(s, 32);
;                         const int head = (u.pn & 3) * 2 + bj;
;                         if (fq == 0) ssq[(size_t)((kind * 8 + head) * 4 + wc) * MT + row] = s;
;                     } else if (kind <= 3) {
;                         const int i0 = (c0 & 127) >> 1;
;                         const f32x4 csa = *(const f32x4*)(cs + (size_t)pos * 64 + i0), csb = *(const f32x4*)(cs + (size_t)pos * 64 + i0 + 2);
;                         const float sc = (kind == 3) ? KSCALE : 1.0f;
;                         f32x4 w0, w1;
;                         w0[0] = (v0[0] * csa[0] - v0[1] * csa[1]) * sc; w0[1] = (v0[1] * csa[0] + v0[0] * csa[1]) * sc;
;                         w0[2] = (v0[2] * csa[2] - v0[3] * csa[3]) * sc; w0[3] = (v0[3] * csa[2] + v0[2] * csa[3]) * sc;
;                         w1[0] = (v1[0] * csb[0] - v1[1] * csb[1]) * sc; w1[1] = (v1[1] * csb[0] + v1[0] * csb[1]) * sc;
;                         w1[2] = (v1[2] * csb[2] - v1[3] * csb[3]) * sc; w1[3] = (v1[3] * csb[2] + v1[2] * csb[3]) * sc;
;                         v0 = w0; v1 = w1;
.LBB0_339:
	s_andn2_b64 vcc, exec, s[0:1]
	s_cbranch_vccnz .LBB0_341
	v_lshlrev_b32_e32 v184, 3, v58
	v_lshl_add_u64 v[42:43], v[136:137], 0, v[184:185]
	v_mov_b32_e32 v46, v180
	v_mov_b32_e32 v47, v181
	v_mov_b32_e32 v48, v182
	v_mov_b32_e32 v49, v183
	v_mov_b32_e32 v42, v176
	v_mov_b32_e32 v43, v177
	v_mov_b32_e32 v44, v178
	v_mov_b32_e32 v45, v179
	v_pk_mul_f32 v[50:51], v[36:37], v[42:43] op_sel:[1,1] op_sel_hi:[0,1]
	v_pk_fma_f32 v[52:53], v[36:37], v[42:43], v[50:51] neg_lo:[0,0,1] neg_hi:[0,0,1]
	v_pk_fma_f32 v[42:43], v[36:37], v[42:43], v[50:51] op_sel_hi:[1,0,1]
	v_mul_f32_e32 v50, v39, v45
	v_mov_b32_e32 v53, v43
	v_pk_mul_f32 v[42:43], v[144:145], v[52:53] op_sel_hi:[0,1]
	v_mul_f32_e32 v52, v39, v44
	v_pk_fma_f32 v[50:51], v[38:39], v[44:45], v[50:51] op_sel_hi:[1,1,0] neg_lo:[0,0,1] neg_hi:[0,0,1]
	v_pk_fma_f32 v[44:45], v[38:39], v[44:45], v[52:53] op_sel:[1,0,0] op_sel_hi:[0,1,0]
	v_mov_b32_e32 v51, v45
	v_pk_mul_f32 v[44:45], v[144:145], v[50:51] op_sel_hi:[0,1]
	v_pk_mul_f32 v[50:51], v[32:33], v[46:47] op_sel:[1,1] op_sel_hi:[0,1]
	v_pk_fma_f32 v[52:53], v[32:33], v[46:47], v[50:51] neg_lo:[0,0,1] neg_hi:[0,0,1]
	v_pk_fma_f32 v[46:47], v[32:33], v[46:47], v[50:51] op_sel_hi:[1,0,1]
	v_mul_f32_e32 v50, v35, v49
	v_mov_b32_e32 v53, v47
	v_pk_mul_f32 v[46:47], v[144:145], v[52:53] op_sel_hi:[0,1]
	v_mul_f32_e32 v52, v35, v48
	v_pk_fma_f32 v[50:51], v[34:35], v[48:49], v[50:51] op_sel_hi:[1,1,0] neg_lo:[0,0,1] neg_hi:[0,0,1]
	v_pk_fma_f32 v[48:49], v[34:35], v[48:49], v[52:53] op_sel:[1,0,0] op_sel_hi:[0,1,0]
	v_mov_b32_e32 v51, v49
	v_pk_mul_f32 v[48:49], v[144:145], v[50:51] op_sel_hi:[0,1]

;     __device__ __forceinline__ void operator()(const f32x4 (&acc)[2][2][4][2], const Unit& u, int wr, int wc, int fr, int fq) const {
;     ...
;                     const int c0 = u.pn * BM + bj * HALF + wc * 32 + 8 * fq;
;                     f32x4 v0 = acc[ai][bj][m][0] * rs, v1 = acc[ai][bj][m][1] * rs;
;                     if (kind <= 1) {
;                         float s = (v0[0] * v0[0] + v0[1] * v0[1]) + (v0[2] * v0[2] + v0[3] * v0[3]) + (v1[0] * v1[0] + v1[1] * v1[1]) + (v1[2] * v1[2] + v1[3] * v1[3]);
;                         s += __shfl_xor(s, 16); s += __shfl_xor(s, 32);
;                         const int head = (u.pn & 3) * 2 + bj;
;                         if (fq == 0) ssq[(size_t)((kind * 8 + head) * 4 + wc) * MT + row] = s;
;                     } else if (kind <= 3) {
;                         const int i0 = (c0 & 127) >> 1;
;                         const f32x4 csa = *(const f32x4*)(cs + (size_t)pos * 64 + i0), csb = *(const f32x4*)(cs + (size_t)pos * 64 + i0 + 2);
;                         const float sc = (kind == 3) ? KSCALE : 1.0f;
;                         f32x4 w0, w1;
;                         w0[0] = (v0[0] * csa[0] - v0[1] * csa[1]) * sc; w0[1] = (v0[1] * csa[0] + v0[0] * csa[1]) * sc;
;                         w0[2] = (v0[2] * csa[2] - v0[3] * csa[3]) * sc; w0[3] = (v0[3] * csa[2] + v0[2] * csa[3]) * sc;
;                         w1[0] = (v1[0] * csb[0] - v1[1] * csb[1]) * sc; w1[1] = (v1[1] * csb[0] + v1[0] * csb[1]) * sc;
;                         w1[2] = (v1[2] * csb[2] - v1[3] * csb[3]) * sc; w1[3] = (v1[3] * csb[2] + v1[2] * csb[3]) * sc;
;                         v0 = w0; v1 = w1;
.LBB0_349:
	s_andn2_b64 vcc, exec, s[0:1]
	s_cbranch_vccnz .LBB0_351
	v_lshlrev_b32_e32 v184, 3, v42
	v_lshl_add_u64 v[34:35], v[136:137], 0, v[184:185]
	s_waitcnt vmcnt(8)
	v_mov_b32_e32 v38, v198
	v_mov_b32_e32 v39, v199
	v_mov_b32_e32 v40, v200
	v_mov_b32_e32 v41, v201
	v_mov_b32_e32 v34, v194
	v_mov_b32_e32 v35, v195
	v_mov_b32_e32 v36, v196
	v_mov_b32_e32 v37, v197
	v_pk_mul_f32 v[44:45], v[28:29], v[34:35] op_sel:[1,1] op_sel_hi:[0,1]
	v_pk_fma_f32 v[46:47], v[28:29], v[34:35], v[44:45] neg_lo:[0,0,1] neg_hi:[0,0,1]
	v_pk_fma_f32 v[34:35], v[28:29], v[34:35], v[44:45] op_sel_hi:[1,0,1]
	v_mul_f32_e32 v44, v31, v37
	v_mov_b32_e32 v47, v35
	v_pk_mul_f32 v[34:35], v[144:145], v[46:47] op_sel_hi:[0,1]
	v_mul_f32_e32 v46, v31, v36
	v_pk_fma_f32 v[44:45], v[30:31], v[36:37], v[44:45] op_sel_hi:[1,1,0] neg_lo:[0,0,1] neg_hi:[0,0,1]
	v_pk_fma_f32 v[36:37], v[30:31], v[36:37], v[46:47] op_sel:[1,0,0] op_sel_hi:[0,1,0]
	v_mov_b32_e32 v45, v37
	v_pk_mul_f32 v[36:37], v[144:145], v[44:45] op_sel_hi:[0,1]
	v_pk_mul_f32 v[44:45], v[24:25], v[38:39] op_sel:[1,1] op_sel_hi:[0,1]
	v_pk_fma_f32 v[46:47], v[24:25], v[38:39], v[44:45] neg_lo:[0,0,1] neg_hi:[0,0,1]
	v_pk_fma_f32 v[38:39], v[24:25], v[38:39], v[44:45] op_sel_hi:[1,0,1]
	v_mul_f32_e32 v44, v27, v41
	v_mov_b32_e32 v47, v39
	v_pk_mul_f32 v[38:39], v[144:145], v[46:47] op_sel_hi:[0,1]
	v_mul_f32_e32 v46, v27, v40
	v_pk_fma_f32 v[44:45], v[26:27], v[40:41], v[44:45] op_sel_hi:[1,1,0] neg_lo:[0,0,1] neg_hi:[0,0,1]
	v_pk_fma_f32 v[40:41], v[26:27], v[40:41], v[46:47] op_sel:[1,0,0] op_sel_hi:[0,1,0]
	v_mov_b32_e32 v45, v41
	v_pk_mul_f32 v[40:41], v[144:145], v[44:45] op_sel_hi:[0,1]

;     __device__ __forceinline__ void operator()(const f32x4 (&acc)[2][2][4][2], const Unit& u, int wr, int wc, int fr, int fq) const {
;     ...
;                     const int c0 = u.pn * BM + bj * HALF + wc * 32 + 8 * fq;
;                     f32x4 v0 = acc[ai][bj][m][0] * rs, v1 = acc[ai][bj][m][1] * rs;
;                     if (kind <= 1) {
;                         float s = (v0[0] * v0[0] + v0[1] * v0[1]) + (v0[2] * v0[2] + v0[3] * v0[3]) + (v1[0] * v1[0] + v1[1] * v1[1]) + (v1[2] * v1[2] + v1[3] * v1[3]);
;                         s += __shfl_xor(s, 16); s += __shfl_xor(s, 32);
;                         const int head = (u.pn & 3) * 2 + bj;
;                         if (fq == 0) ssq[(size_t)((kind * 8 + head) * 4 + wc) * MT + row] = s;
;                     } else if (kind <= 3) {
;                         const int i0 = (c0 & 127) >> 1;
;                         const f32x4 csa = *(const f32x4*)(cs + (size_t)pos * 64 + i0), csb = *(const f32x4*)(cs + (size_t)pos * 64 + i0 + 2);
;                         const float sc = (kind == 3) ? KSCALE : 1.0f;
;                         f32x4 w0, w1;
;                         w0[0] = (v0[0] * csa[0] - v0[1] * csa[1]) * sc; w0[1] = (v0[1] * csa[0] + v0[0] * csa[1]) * sc;
;                         w0[2] = (v0[2] * csa[2] - v0[3] * csa[3]) * sc; w0[3] = (v0[3] * csa[2] + v0[2] * csa[3]) * sc;
;                         w1[0] = (v1[0] * csb[0] - v1[1] * csb[1]) * sc; w1[1] = (v1[1] * csb[0] + v1[0] * csb[1]) * sc;
;                         w1[2] = (v1[2] * csb[2] - v1[3] * csb[3]) * sc; w1[3] = (v1[3] * csb[2] + v1[2] * csb[3]) * sc;
;                         v0 = w0; v1 = w1;
.LBB0_359:
	s_andn2_b64 vcc, exec, s[0:1]
	s_cbranch_vccnz .LBB0_361
	v_lshlrev_b32_e32 v184, 3, v42
	v_lshl_add_u64 v[26:27], v[136:137], 0, v[184:185]
	v_mov_b32_e32 v30, v198
	v_mov_b32_e32 v31, v199
	v_mov_b32_e32 v32, v200
	v_mov_b32_e32 v33, v201
	v_mov_b32_e32 v26, v194
	v_mov_b32_e32 v27, v195
	v_mov_b32_e32 v28, v196
	v_mov_b32_e32 v29, v197
	v_pk_mul_f32 v[34:35], v[20:21], v[26:27] op_sel:[1,1] op_sel_hi:[0,1]
	v_pk_fma_f32 v[36:37], v[20:21], v[26:27], v[34:35] neg_lo:[0,0,1] neg_hi:[0,0,1]
	v_pk_fma_f32 v[26:27], v[20:21], v[26:27], v[34:35] op_sel_hi:[1,0,1]
	v_mul_f32_e32 v34, v23, v29
	v_mov_b32_e32 v37, v27
	v_pk_mul_f32 v[26:27], v[144:145], v[36:37] op_sel_hi:[0,1]
	v_mul_f32_e32 v36, v23, v28
	v_pk_fma_f32 v[34:35], v[22:23], v[28:29], v[34:35] op_sel_hi:[1,1,0] neg_lo:[0,0,1] neg_hi:[0,0,1]
	v_pk_fma_f32 v[28:29], v[22:23], v[28:29], v[36:37] op_sel:[1,0,0] op_sel_hi:[0,1,0]
	v_mov_b32_e32 v35, v29
	v_pk_mul_f32 v[28:29], v[144:145], v[34:35] op_sel_hi:[0,1]
	v_pk_mul_f32 v[34:35], v[16:17], v[30:31] op_sel:[1,1] op_sel_hi:[0,1]
	v_pk_fma_f32 v[36:37], v[16:17], v[30:31], v[34:35] neg_lo:[0,0,1] neg_hi:[0,0,1]
	v_pk_fma_f32 v[30:31], v[16:17], v[30:31], v[34:35] op_sel_hi:[1,0,1]
	v_mul_f32_e32 v34, v19, v33
	v_mov_b32_e32 v37, v31
	v_pk_mul_f32 v[30:31], v[144:145], v[36:37] op_sel_hi:[0,1]
	v_mul_f32_e32 v36, v19, v32
	v_pk_fma_f32 v[34:35], v[18:19], v[32:33], v[34:35] op_sel_hi:[1,1,0] neg_lo:[0,0,1] neg_hi:[0,0,1]
	v_pk_fma_f32 v[32:33], v[18:19], v[32:33], v[36:37] op_sel:[1,0,0] op_sel_hi:[0,1,0]
	v_mov_b32_e32 v35, v33
	v_pk_mul_f32 v[32:33], v[144:145], v[34:35] op_sel_hi:[0,1]

;     __device__ __forceinline__ void operator()(const f32x4 (&acc)[2][2][4][2], const Unit& u, int wr, int wc, int fr, int fq) const {
;     ...
;                     const int c0 = u.pn * BM + bj * HALF + wc * 32 + 8 * fq;
;                     f32x4 v0 = acc[ai][bj][m][0] * rs, v1 = acc[ai][bj][m][1] * rs;
;                     if (kind <= 1) {
;                         float s = (v0[0] * v0[0] + v0[1] * v0[1]) + (v0[2] * v0[2] + v0[3] * v0[3]) + (v1[0] * v1[0] + v1[1] * v1[1]) + (v1[2] * v1[2] + v1[3] * v1[3]);
;                         s += __shfl_xor(s, 16); s += __shfl_xor(s, 32);
;                         const int head = (u.pn & 3) * 2 + bj;
;                         if (fq == 0) ssq[(size_t)((kind * 8 + head) * 4 + wc) * MT + row] = s;
;                     } else if (kind <= 3) {
;                         const int i0 = (c0 & 127) >> 1;
;                         const f32x4 csa = *(const f32x4*)(cs + (size_t)pos * 64 + i0), csb = *(const f32x4*)(cs + (size_t)pos * 64 + i0 + 2);
;                         const float sc = (kind == 3) ? KSCALE : 1.0f;
;                         f32x4 w0, w1;
;                         w0[0] = (v0[0] * csa[0] - v0[1] * csa[1]) * sc; w0[1] = (v0[1] * csa[0] + v0[0] * csa[1]) * sc;
;                         w0[2] = (v0[2] * csa[2] - v0[3] * csa[3]) * sc; w0[3] = (v0[3] * csa[2] + v0[2] * csa[3]) * sc;
;                         w1[0] = (v1[0] * csb[0] - v1[1] * csb[1]) * sc; w1[1] = (v1[1] * csb[0] + v1[0] * csb[1]) * sc;
;                         w1[2] = (v1[2] * csb[2] - v1[3] * csb[3]) * sc; w1[3] = (v1[3] * csb[2] + v1[2] * csb[3]) * sc;
;                         v0 = w0; v1 = w1;
.LBB0_369:
	s_andn2_b64 vcc, exec, s[0:1]
	s_cbranch_vccnz .LBB0_371
	v_lshlrev_b32_e32 v184, 3, v26
	v_lshl_add_u64 v[18:19], v[136:137], 0, v[184:185]
	s_waitcnt vmcnt(6)
	v_mov_b32_e32 v22, v206
	v_mov_b32_e32 v23, v207
	v_mov_b32_e32 v24, v208
	v_mov_b32_e32 v25, v209
	v_mov_b32_e32 v18, v202
	v_mov_b32_e32 v19, v203
	v_mov_b32_e32 v20, v204
	v_mov_b32_e32 v21, v205
	v_pk_mul_f32 v[28:29], v[12:13], v[18:19] op_sel:[1,1] op_sel_hi:[0,1]
	v_pk_fma_f32 v[30:31], v[12:13], v[18:19], v[28:29] neg_lo:[0,0,1] neg_hi:[0,0,1]
	v_pk_fma_f32 v[18:19], v[12:13], v[18:19], v[28:29] op_sel_hi:[1,0,1]
	v_mul_f32_e32 v28, v15, v21
	v_mov_b32_e32 v31, v19
	v_pk_mul_f32 v[18:19], v[144:145], v[30:31] op_sel_hi:[0,1]
	v_mul_f32_e32 v30, v15, v20
	v_pk_fma_f32 v[28:29], v[14:15], v[20:21], v[28:29] op_sel_hi:[1,1,0] neg_lo:[0,0,1] neg_hi:[0,0,1]
	v_pk_fma_f32 v[20:21], v[14:15], v[20:21], v[30:31] op_sel:[1,0,0] op_sel_hi:[0,1,0]
	v_mov_b32_e32 v29, v21
	v_pk_mul_f32 v[20:21], v[144:145], v[28:29] op_sel_hi:[0,1]
	v_pk_mul_f32 v[28:29], v[8:9], v[22:23] op_sel:[1,1] op_sel_hi:[0,1]
	v_pk_fma_f32 v[30:31], v[8:9], v[22:23], v[28:29] neg_lo:[0,0,1] neg_hi:[0,0,1]
	v_pk_fma_f32 v[22:23], v[8:9], v[22:23], v[28:29] op_sel_hi:[1,0,1]
	v_mul_f32_e32 v28, v11, v25
	v_mov_b32_e32 v31, v23
	v_pk_mul_f32 v[22:23], v[144:145], v[30:31] op_sel_hi:[0,1]
	v_mul_f32_e32 v30, v11, v24
	v_pk_fma_f32 v[28:29], v[10:11], v[24:25], v[28:29] op_sel_hi:[1,1,0] neg_lo:[0,0,1] neg_hi:[0,0,1]
	v_pk_fma_f32 v[24:25], v[10:11], v[24:25], v[30:31] op_sel:[1,0,0] op_sel_hi:[0,1,0]
	v_mov_b32_e32 v29, v25
	v_pk_mul_f32 v[24:25], v[144:145], v[28:29] op_sel_hi:[0,1]

;     __device__ __forceinline__ void operator()(const f32x4 (&acc)[2][2][4][2], const Unit& u, int wr, int wc, int fr, int fq) const {
;     ...
;                     const int c0 = u.pn * BM + bj * HALF + wc * 32 + 8 * fq;
;                     f32x4 v0 = acc[ai][bj][m][0] * rs, v1 = acc[ai][bj][m][1] * rs;
;                     if (kind <= 1) {
;                         float s = (v0[0] * v0[0] + v0[1] * v0[1]) + (v0[2] * v0[2] + v0[3] * v0[3]) + (v1[0] * v1[0] + v1[1] * v1[1]) + (v1[2] * v1[2] + v1[3] * v1[3]);
;                         s += __shfl_xor(s, 16); s += __shfl_xor(s, 32);
;                         const int head = (u.pn & 3) * 2 + bj;
;                         if (fq == 0) ssq[(size_t)((kind * 8 + head) * 4 + wc) * MT + row] = s;
;                     } else if (kind <= 3) {
;                         const int i0 = (c0 & 127) >> 1;
;                         const f32x4 csa = *(const f32x4*)(cs + (size_t)pos * 64 + i0), csb = *(const f32x4*)(cs + (size_t)pos * 64 + i0 + 2);
;                         const float sc = (kind == 3) ? KSCALE : 1.0f;
;                         f32x4 w0, w1;
;                         w0[0] = (v0[0] * csa[0] - v0[1] * csa[1]) * sc; w0[1] = (v0[1] * csa[0] + v0[0] * csa[1]) * sc;
;                         w0[2] = (v0[2] * csa[2] - v0[3] * csa[3]) * sc; w0[3] = (v0[3] * csa[2] + v0[2] * csa[3]) * sc;
;                         w1[0] = (v1[0] * csb[0] - v1[1] * csb[1]) * sc; w1[1] = (v1[1] * csb[0] + v1[0] * csb[1]) * sc;
;                         w1[2] = (v1[2] * csb[2] - v1[3] * csb[3]) * sc; w1[3] = (v1[3] * csb[2] + v1[2] * csb[3]) * sc;
;                         v0 = w0; v1 = w1;
.LBB0_379:
	s_andn2_b64 vcc, exec, s[0:1]
	s_cbranch_vccnz .LBB0_381
	v_lshlrev_b32_e32 v184, 3, v26
	v_lshl_add_u64 v[10:11], v[136:137], 0, v[184:185]
	v_mov_b32_e32 v14, v206
	v_mov_b32_e32 v15, v207
	v_mov_b32_e32 v16, v208
	v_mov_b32_e32 v17, v209
	v_mov_b32_e32 v10, v202
	v_mov_b32_e32 v11, v203
	v_mov_b32_e32 v12, v204
	v_mov_b32_e32 v13, v205
	v_pk_mul_f32 v[18:19], v[4:5], v[10:11] op_sel:[1,1] op_sel_hi:[0,1]
	v_pk_fma_f32 v[20:21], v[4:5], v[10:11], v[18:19] neg_lo:[0,0,1] neg_hi:[0,0,1]
	v_pk_fma_f32 v[10:11], v[4:5], v[10:11], v[18:19] op_sel_hi:[1,0,1]
	v_mul_f32_e32 v18, v7, v13
	v_mov_b32_e32 v21, v11
	v_pk_mul_f32 v[10:11], v[144:145], v[20:21] op_sel_hi:[0,1]
	v_mul_f32_e32 v20, v7, v12
	v_pk_fma_f32 v[18:19], v[6:7], v[12:13], v[18:19] op_sel_hi:[1,1,0] neg_lo:[0,0,1] neg_hi:[0,0,1]
	v_pk_fma_f32 v[12:13], v[6:7], v[12:13], v[20:21] op_sel:[1,0,0] op_sel_hi:[0,1,0]
	v_mov_b32_e32 v19, v13
	v_pk_mul_f32 v[12:13], v[144:145], v[18:19] op_sel_hi:[0,1]
	v_pk_mul_f32 v[18:19], v[0:1], v[14:15] op_sel:[1,1] op_sel_hi:[0,1]
	v_pk_fma_f32 v[20:21], v[0:1], v[14:15], v[18:19] neg_lo:[0,0,1] neg_hi:[0,0,1]
	v_pk_fma_f32 v[14:15], v[0:1], v[14:15], v[18:19] op_sel_hi:[1,0,1]
	v_mul_f32_e32 v18, v3, v17
	v_mov_b32_e32 v21, v15
	v_pk_mul_f32 v[14:15], v[144:145], v[20:21] op_sel_hi:[0,1]
	v_mul_f32_e32 v20, v3, v16
	v_pk_fma_f32 v[18:19], v[2:3], v[16:17], v[18:19] op_sel_hi:[1,1,0] neg_lo:[0,0,1] neg_hi:[0,0,1]
	v_pk_fma_f32 v[16:17], v[2:3], v[16:17], v[20:21] op_sel:[1,0,0] op_sel_hi:[0,1,0]
	v_mov_b32_e32 v19, v17
	v_pk_mul_f32 v[16:17], v[144:145], v[18:19] op_sel_hi:[0,1]

; __device__ __forceinline__ unsigned cvt_pk_bf16(float lo, float hi) { unsigned r; asm volatile("v_cvt_pk_bf16_f32 %0, %1, %2" : "=v"(r) : "v"(lo), "v"(hi)); return r; }
;     __device__ __forceinline__ void operator()(const f32x4 (&acc)[2][2][4][2], const Unit& u, int wr, int wc, int fr, int fq) const {
;         const int row0 = u.pm * BM + wr * 64 + fr, col0 = u.pn * BM + wc * 32 + 4 * fq;
; #pragma unroll
;         for (int ai = 0; ai < 2; ++ai)
; #pragma unroll
;             for (int m = 0; m < 4; ++m) { const int row = row0 + ai * HALF + m * 16; const size_t ro = (size_t)row * 2048 + col0;
;                 float s = 0.f;
; #pragma unroll
;                 for (int bj = 0; bj < 2; ++bj)
; #pragma unroll
;                     for (int n = 0; n < 2; ++n) { f32x4 r;
;                         if (R32) r = *(const f32x4*)(R32 + ro + bj * HALF + n * 16);
;                         else { typedef unsigned u32x2_t __attribute__((ext_vector_type(2))); const u32x2_t rw = *(const u32x2_t*)(R16 + ro + bj * HALF + n * 16); const unsigned r0 = rw.x, r1 = rw.y;
;                             r = (f32x4){__builtin_bit_cast(float, r0 << 16), __builtin_bit_cast(float, r0 & 0xffff0000u), __builtin_bit_cast(float, r1 << 16), __builtin_bit_cast(float, r1 & 0xffff0000u)}; }
;                         const f32x4 v = acc[ai][bj][m][n] + r;
;                         typedef unsigned u32x2_s __attribute__((ext_vector_type(2))); u32x2_s w; w.x = cvt_pk_bf16(v[0], v[1]); w.y = cvt_pk_bf16(v[2], v[3]);
;                         *(u32x2_s*)(XB + ro + bj * HALF + n * 16) = w;
;                         s += (v[0] * v[0] + v[1] * v[1]) + (v[2] * v[2] + v[3] * v[3]); }
;                 s += __shfl_xor(s, 16); s += __shfl_xor(s, 32);
;                 if (fq == 0) ss2[(size_t)(u.pn * 4 + wc) * MT + row] = s; }
.LBB0_728:
	v_lshl_add_u32 v138, s40, 8, v152
	v_lshl_or_b32 v142, s64, 8, v154
	v_ashrrev_i32_e32 v139, 31, v138
	v_ashrrev_i32_e32 v143, 31, v142
	v_lshlrev_b64 v[128:129], 11, v[138:139]
	v_readlane_b32 s4, v252, 2
	v_lshl_add_u64 v[140:141], v[128:129], 0, v[142:143]
	v_cndmask_b32_e64 v128, 0, 1, s[88:89]
	v_readlane_b32 s5, v252, 3
	s_mov_b64 s[2:3], -1
	v_cmp_ne_u32_e64 s[40:41], 1, v128
	s_andn2_b64 vcc, exec, s[88:89]
	v_lshl_add_u64 v[144:145], v[140:141], 2, s[4:5]
	v_readlane_b32 s58, v250, 24
	v_readlane_b32 s68, v250, 25
	v_readlane_b32 s66, v250, 30
	v_readlane_b32 s6, v252, 4
	v_readlane_b32 s7, v252, 5
	v_readlane_b32 s8, v252, 6
	v_readlane_b32 s9, v252, 7
	v_readlane_b32 s10, v252, 8
	v_readlane_b32 s11, v252, 9
	v_readlane_b32 s12, v252, 10
	v_readlane_b32 s13, v252, 11
	v_readlane_b32 s14, v252, 12
	v_readlane_b32 s15, v252, 13
	v_readlane_b32 s16, v252, 14
	v_readlane_b32 s17, v252, 15
	v_readlane_b32 s18, v252, 16
	v_readlane_b32 s19, v252, 17
	s_cbranch_vccnz .LBB0_730
	global_load_dwordx4 v[128:131], v[144:145], off
	s_waitcnt vmcnt(0)
	s_mov_b64 s[2:3], 0
.LBB0_730:
	s_andn2_b64 vcc, exec, s[2:3]
	v_lshl_add_u64 v[146:147], v[140:141], 1, s[48:49]
	s_cbranch_vccnz .LBB0_732
	v_mov_b32_e32 v204, v146
	v_mov_b32_e32 v205, v147
	global_load_dwordx2 v[156:157], v[204:205], off
	global_load_dwordx2 v[158:159], v[204:205], off offset:32
	global_load_dwordx2 v[160:161], v[204:205], off offset:256
	global_load_dwordx2 v[162:163], v[204:205], off offset:288
	s_mov_b32 s100, 0x10000
	s_mov_b32 s101, 0
	v_lshl_add_u64 v[202:203], v[204:205], 0, s[100:101]
	global_load_dwordx2 v[164:165], v[202:203], off
	global_load_dwordx2 v[166:167], v[202:203], off offset:32
	global_load_dwordx2 v[168:169], v[202:203], off offset:256
	global_load_dwordx2 v[170:171], v[202:203], off offset:288
	s_mov_b32 s100, 0x20000
	s_mov_b32 s101, 0
	v_lshl_add_u64 v[202:203], v[204:205], 0, s[100:101]
	global_load_dwordx2 v[172:173], v[202:203], off
	global_load_dwordx2 v[174:175], v[202:203], off offset:32
	global_load_dwordx2 v[176:177], v[202:203], off offset:256
	global_load_dwordx2 v[178:179], v[202:203], off offset:288
	s_mov_b32 s100, 0x30000
	s_mov_b32 s101, 0
	v_lshl_add_u64 v[202:203], v[204:205], 0, s[100:101]
	global_load_dwordx2 v[194:195], v[202:203], off
	global_load_dwordx2 v[196:197], v[202:203], off offset:32
	global_load_dwordx2 v[198:199], v[202:203], off offset:256
	global_load_dwordx2 v[200:201], v[202:203], off offset:288
	s_waitcnt vmcnt(12)
	v_lshlrev_b32_e32 v128, 16, v156
	v_and_b32_e32 v129, 0xffff0000, v156
	v_lshlrev_b32_e32 v130, 16, v157
	v_and_b32_e32 v131, 0xffff0000, v157
.LBB0_732:
	v_pk_add_f32 v[130:131], v[126:127], v[130:131]
	v_pk_add_f32 v[148:149], v[124:125], v[128:129]
	v_lshl_add_u64 v[128:129], v[140:141], 1, s[90:91]
	v_cvt_pk_bf16_f32 v124, v148, v149
	v_cvt_pk_bf16_f32 v125, v130, v131
	s_and_b64 vcc, exec, s[40:41]
	s_mov_b64 s[2:3], -1
	global_store_dwordx2 v[128:129], v[124:125], off
	s_cbranch_vccnz .LBB0_734
	global_load_dwordx4 v[124:127], v[144:145], off offset:64
	s_waitcnt vmcnt(0)
	s_mov_b64 s[2:3], 0
.LBB0_734:
	s_andn2_b64 vcc, exec, s[2:3]
	s_cbranch_vccnz .LBB0_736
	v_lshlrev_b32_e32 v124, 16, v158
	v_and_b32_e32 v125, 0xffff0000, v158
	v_lshlrev_b32_e32 v126, 16, v159
	v_and_b32_e32 v127, 0xffff0000, v159
.LBB0_736:
	v_pk_add_f32 v[126:127], v[122:123], v[126:127]
	v_pk_add_f32 v[124:125], v[120:121], v[124:125]
	s_and_b64 vcc, exec, s[40:41]
	v_cvt_pk_bf16_f32 v120, v124, v125
	v_cvt_pk_bf16_f32 v121, v126, v127
	s_mov_b64 s[2:3], -1
	global_store_dwordx2 v[128:129], v[120:121], off offset:32
	s_cbranch_vccnz .LBB0_738
	global_load_dwordx4 v[120:123], v[144:145], off offset:512
	s_waitcnt vmcnt(0)
	s_mov_b64 s[2:3], 0
.LBB0_738:
	s_andn2_b64 vcc, exec, s[2:3]
	s_cbranch_vccnz .LBB0_740
	v_lshlrev_b32_e32 v120, 16, v160
	v_and_b32_e32 v121, 0xffff0000, v160
	v_lshlrev_b32_e32 v122, 16, v161
	v_and_b32_e32 v123, 0xffff0000, v161
.LBB0_740:
	v_pk_add_f32 v[122:123], v[118:119], v[122:123]
	v_pk_add_f32 v[120:121], v[116:117], v[120:121]
	s_and_b64 vcc, exec, s[40:41]
	v_cvt_pk_bf16_f32 v116, v120, v121
	v_cvt_pk_bf16_f32 v117, v122, v123
	s_mov_b64 s[2:3], -1
	global_store_dwordx2 v[128:129], v[116:117], off offset:256
	s_cbranch_vccnz .LBB0_742
	global_load_dwordx4 v[116:119], v[144:145], off offset:576
	s_waitcnt vmcnt(0)
	s_mov_b64 s[2:3], 0
.LBB0_742:
	s_andn2_b64 vcc, exec, s[2:3]
	s_cbranch_vccnz .LBB0_744
	v_lshlrev_b32_e32 v116, 16, v162
	v_and_b32_e32 v117, 0xffff0000, v162
	v_lshlrev_b32_e32 v118, 16, v163
	v_and_b32_e32 v119, 0xffff0000, v163
.LBB0_744:
	v_mul_f32_e32 v125, v125, v125
	v_mul_f32_e32 v144, v149, v149
	v_mul_f32_e32 v131, v131, v131
	v_fmac_f32_e32 v125, v124, v124
	v_mul_f32_e32 v124, v127, v127
	v_mul_f32_e32 v121, v121, v121
	v_fmac_f32_e32 v144, v148, v148
	v_fmac_f32_e32 v131, v130, v130
	v_fmac_f32_e32 v124, v126, v126
	v_fmac_f32_e32 v121, v120, v120
	v_mul_f32_e32 v120, v123, v123
	v_pk_add_f32 v[114:115], v[114:115], v[118:119]
	v_pk_add_f32 v[116:117], v[112:113], v[116:117]
	v_add_f32_e32 v130, v144, v131
	v_add_f32_e32 v124, v125, v124
	v_fmac_f32_e32 v120, v122, v122
	v_mul_f32_e32 v112, v117, v117
	v_mul_f32_e32 v113, v115, v115
	v_add_f32_e32 v124, v130, v124
	v_add_f32_e32 v120, v121, v120
	v_fmac_f32_e32 v112, v116, v116
	v_fmac_f32_e32 v113, v114, v114
	v_add_f32_e32 v120, v124, v120
	v_add_f32_e32 v112, v112, v113
	v_add_f32_e32 v112, v120, v112
	ds_bpermute_b32 v113, v150, v112
	s_lshl_b32 s2, s64, 2
	s_or_b32 s2, s2, s53
	s_ashr_i32 s3, s2, 31
	s_lshl_b64 s[24:25], s[2:3], 16
	s_waitcnt lgkmcnt(0)
	v_add_f32_e32 v112, v112, v113
	ds_bpermute_b32 v113, v151, v112
	v_cvt_pk_bf16_f32 v116, v116, v117
	v_cvt_pk_bf16_f32 v117, v114, v115
	global_store_dwordx2 v[128:129], v[116:117], off offset:288
	s_and_saveexec_b64 s[2:3], s[36:37]
	s_cbranch_execz .LBB0_746
	v_readlane_b32 s4, v250, 32
	v_readlane_b32 s5, v250, 33
	s_add_u32 s4, s4, s24
	s_addc_u32 s5, s5, s25
	v_lshl_add_u64 v[114:115], v[138:139], 2, s[4:5]
	s_waitcnt lgkmcnt(0)
	v_add_f32_e32 v112, v112, v113
	global_store_dword v[114:115], v112, off
; __device__ __forceinline__ unsigned cvt_pk_bf16(float lo, float hi) { unsigned r; asm volatile("v_cvt_pk_bf16_f32 %0, %1, %2" : "=v"(r) : "v"(lo), "v"(hi)); return r; }
;     __device__ __forceinline__ void operator()(const f32x4 (&acc)[2][2][4][2], const Unit& u, int wr, int wc, int fr, int fq) const {
;         const int row0 = u.pm * BM + wr * 64 + fr, col0 = u.pn * BM + wc * 32 + 4 * fq;
; #pragma unroll
;         for (int ai = 0; ai < 2; ++ai)
; #pragma unroll
;             for (int m = 0; m < 4; ++m) { const int row = row0 + ai * HALF + m * 16; const size_t ro = (size_t)row * 2048 + col0;
;                 float s = 0.f;
; #pragma unroll
;                 for (int bj = 0; bj < 2; ++bj)
; #pragma unroll
;                     for (int n = 0; n < 2; ++n) { f32x4 r;
;                         if (R32) r = *(const f32x4*)(R32 + ro + bj * HALF + n * 16);
;                         else { typedef unsigned u32x2_t __attribute__((ext_vector_type(2))); const u32x2_t rw = *(const u32x2_t*)(R16 + ro + bj * HALF + n * 16); const unsigned r0 = rw.x, r1 = rw.y;
;                             r = (f32x4){__builtin_bit_cast(float, r0 << 16), __builtin_bit_cast(float, r0 & 0xffff0000u), __builtin_bit_cast(float, r1 << 16), __builtin_bit_cast(float, r1 & 0xffff0000u)}; }
;                         const f32x4 v = acc[ai][bj][m][n] + r;
;                         typedef unsigned u32x2_s __attribute__((ext_vector_type(2))); u32x2_s w; w.x = cvt_pk_bf16(v[0], v[1]); w.y = cvt_pk_bf16(v[2], v[3]);
;                         *(u32x2_s*)(XB + ro + bj * HALF + n * 16) = w;
;                         s += (v[0] * v[0] + v[1] * v[1]) + (v[2] * v[2] + v[3] * v[3]); }
;                 s += __shfl_xor(s, 16); s += __shfl_xor(s, 32);
;                 if (fq == 0) ss2[(size_t)(u.pn * 4 + wc) * MT + row] = s; }
.LBB0_746:
	s_or_b64 exec, exec, s[2:3]
	v_or_b32_e32 v112, 16, v138
	s_waitcnt lgkmcnt(0)
	v_ashrrev_i32_e32 v113, 31, v112
	v_lshlrev_b64 v[112:113], 11, v[112:113]
	v_readlane_b32 s4, v252, 2
	v_lshl_add_u64 v[122:123], v[112:113], 0, v[142:143]
	v_readlane_b32 s5, v252, 3
	s_mov_b64 s[2:3], -1
	s_and_b64 vcc, exec, s[40:41]
	v_lshl_add_u64 v[116:117], v[122:123], 2, s[4:5]
	v_readlane_b32 s6, v252, 4
	v_readlane_b32 s7, v252, 5
	v_readlane_b32 s8, v252, 6
	v_readlane_b32 s9, v252, 7
	v_readlane_b32 s10, v252, 8
	v_readlane_b32 s11, v252, 9
	v_readlane_b32 s12, v252, 10
	v_readlane_b32 s13, v252, 11
	v_readlane_b32 s14, v252, 12
	v_readlane_b32 s15, v252, 13
	v_readlane_b32 s16, v252, 14
	v_readlane_b32 s17, v252, 15
	v_readlane_b32 s18, v252, 16
	v_readlane_b32 s19, v252, 17
	s_cbranch_vccnz .LBB0_748
	global_load_dwordx4 v[112:115], v[116:117], off
	s_waitcnt vmcnt(0)
	s_mov_b64 s[2:3], 0
.LBB0_748:
	s_andn2_b64 vcc, exec, s[2:3]
	v_lshl_add_u64 v[118:119], v[122:123], 1, s[48:49]
	s_cbranch_vccnz .LBB0_750
	s_mov_b32 s100, 0x80000
	s_mov_b32 s101, 0
	v_lshl_add_u64 v[202:203], v[204:205], 0, s[100:101]
	global_load_dwordx2 v[156:157], v[202:203], off
	global_load_dwordx2 v[158:159], v[202:203], off offset:32
	global_load_dwordx2 v[160:161], v[202:203], off offset:256
	global_load_dwordx2 v[162:163], v[202:203], off offset:288
	s_waitcnt vmcnt(16)
	v_lshlrev_b32_e32 v112, 16, v164
	v_and_b32_e32 v113, 0xffff0000, v164
	v_lshlrev_b32_e32 v114, 16, v165
	v_and_b32_e32 v115, 0xffff0000, v165
.LBB0_750:
	v_pk_add_f32 v[114:115], v[110:111], v[114:115]
	v_pk_add_f32 v[120:121], v[108:109], v[112:113]
	v_lshl_add_u64 v[112:113], v[122:123], 1, s[90:91]
	v_cvt_pk_bf16_f32 v108, v120, v121
	v_cvt_pk_bf16_f32 v109, v114, v115
	s_and_b64 vcc, exec, s[40:41]
	s_mov_b64 s[2:3], -1
	global_store_dwordx2 v[112:113], v[108:109], off
	s_cbranch_vccnz .LBB0_752
	global_load_dwordx4 v[108:111], v[116:117], off offset:64
	s_waitcnt vmcnt(0)
	s_mov_b64 s[2:3], 0
.LBB0_752:
	s_andn2_b64 vcc, exec, s[2:3]
	s_cbranch_vccnz .LBB0_754
	v_lshlrev_b32_e32 v108, 16, v166
	v_and_b32_e32 v109, 0xffff0000, v166
	v_lshlrev_b32_e32 v110, 16, v167
	v_and_b32_e32 v111, 0xffff0000, v167
.LBB0_754:
	v_pk_add_f32 v[110:111], v[106:107], v[110:111]
	v_pk_add_f32 v[108:109], v[104:105], v[108:109]
	s_and_b64 vcc, exec, s[40:41]
	v_cvt_pk_bf16_f32 v104, v108, v109
	v_cvt_pk_bf16_f32 v105, v110, v111
	s_mov_b64 s[2:3], -1
	global_store_dwordx2 v[112:113], v[104:105], off offset:32
	s_cbranch_vccnz .LBB0_756
	global_load_dwordx4 v[104:107], v[116:117], off offset:512
	s_waitcnt vmcnt(0)
	s_mov_b64 s[2:3], 0
.LBB0_756:
	s_andn2_b64 vcc, exec, s[2:3]
	s_cbranch_vccnz .LBB0_758
	v_lshlrev_b32_e32 v104, 16, v168
	v_and_b32_e32 v105, 0xffff0000, v168
	v_lshlrev_b32_e32 v106, 16, v169
	v_and_b32_e32 v107, 0xffff0000, v169
.LBB0_758:
	v_pk_add_f32 v[106:107], v[102:103], v[106:107]
	v_pk_add_f32 v[104:105], v[100:101], v[104:105]
	s_and_b64 vcc, exec, s[40:41]
	v_cvt_pk_bf16_f32 v100, v104, v105
	v_cvt_pk_bf16_f32 v101, v106, v107
	s_mov_b64 s[2:3], -1
	global_store_dwordx2 v[112:113], v[100:101], off offset:256
	s_cbranch_vccnz .LBB0_760
	global_load_dwordx4 v[100:103], v[116:117], off offset:576
	s_waitcnt vmcnt(0)
	s_mov_b64 s[2:3], 0
.LBB0_760:
	s_andn2_b64 vcc, exec, s[2:3]
	s_cbranch_vccnz .LBB0_762
	v_lshlrev_b32_e32 v100, 16, v170
	v_and_b32_e32 v101, 0xffff0000, v170
	v_lshlrev_b32_e32 v102, 16, v171
	v_and_b32_e32 v103, 0xffff0000, v171
.LBB0_762:
	v_mul_f32_e32 v109, v109, v109
	v_mul_f32_e32 v116, v121, v121
	v_mul_f32_e32 v115, v115, v115
	v_fmac_f32_e32 v109, v108, v108
	v_mul_f32_e32 v108, v111, v111
	v_mul_f32_e32 v105, v105, v105
	v_fmac_f32_e32 v116, v120, v120
	v_fmac_f32_e32 v115, v114, v114
	v_fmac_f32_e32 v108, v110, v110
	v_fmac_f32_e32 v105, v104, v104
	v_mul_f32_e32 v104, v107, v107
	v_pk_add_f32 v[98:99], v[98:99], v[102:103]
	v_pk_add_f32 v[100:101], v[96:97], v[100:101]
	v_add_f32_e32 v114, v116, v115
	v_add_f32_e32 v108, v109, v108
	v_fmac_f32_e32 v104, v106, v106
	v_mul_f32_e32 v96, v101, v101
	v_mul_f32_e32 v97, v99, v99
	v_add_f32_e32 v108, v114, v108
	v_add_f32_e32 v104, v105, v104
	v_fmac_f32_e32 v96, v100, v100
	v_fmac_f32_e32 v97, v98, v98
	v_add_f32_e32 v104, v108, v104
	v_add_f32_e32 v96, v96, v97
	v_add_f32_e32 v96, v104, v96
	ds_bpermute_b32 v97, v150, v96
	v_cvt_pk_bf16_f32 v100, v100, v101
	v_cvt_pk_bf16_f32 v101, v98, v99
	global_store_dwordx2 v[112:113], v[100:101], off offset:288
	s_waitcnt lgkmcnt(0)
	v_add_f32_e32 v96, v96, v97
	ds_bpermute_b32 v97, v151, v96
	s_and_saveexec_b64 s[2:3], s[36:37]
	s_cbranch_execz .LBB0_764
	v_readlane_b32 s4, v250, 32
	v_readlane_b32 s5, v250, 33
	s_add_u32 s4, s4, s24
	s_addc_u32 s5, s5, s25
	v_lshl_add_u64 v[98:99], v[138:139], 2, s[4:5]
	s_waitcnt lgkmcnt(0)
	v_add_f32_e32 v96, v96, v97
	global_store_dword v[98:99], v96, off offset:64
.LBB0_764:
	s_or_b64 exec, exec, s[2:3]
	v_or_b32_e32 v96, 32, v138
	s_waitcnt lgkmcnt(0)
	v_ashrrev_i32_e32 v97, 31, v96
	v_lshlrev_b64 v[96:97], 11, v[96:97]
	v_readlane_b32 s4, v252, 2
	v_lshl_add_u64 v[106:107], v[96:97], 0, v[142:143]
	v_readlane_b32 s5, v252, 3
	s_mov_b64 s[2:3], -1
	s_and_b64 vcc, exec, s[40:41]
	v_lshl_add_u64 v[100:101], v[106:107], 2, s[4:5]
	v_readlane_b32 s6, v252, 4
	v_readlane_b32 s7, v252, 5
	v_readlane_b32 s8, v252, 6
	v_readlane_b32 s9, v252, 7
	v_readlane_b32 s10, v252, 8
	v_readlane_b32 s11, v252, 9
	v_readlane_b32 s12, v252, 10
	v_readlane_b32 s13, v252, 11
	v_readlane_b32 s14, v252, 12
	v_readlane_b32 s15, v252, 13
	v_readlane_b32 s16, v252, 14
	v_readlane_b32 s17, v252, 15
	v_readlane_b32 s18, v252, 16
	v_readlane_b32 s19, v252, 17
	s_cbranch_vccnz .LBB0_766
	global_load_dwordx4 v[96:99], v[100:101], off
	s_waitcnt vmcnt(0)
	s_mov_b64 s[2:3], 0
; __device__ __forceinline__ unsigned cvt_pk_bf16(float lo, float hi) { unsigned r; asm volatile("v_cvt_pk_bf16_f32 %0, %1, %2" : "=v"(r) : "v"(lo), "v"(hi)); return r; }
;     __device__ __forceinline__ void operator()(const f32x4 (&acc)[2][2][4][2], const Unit& u, int wr, int wc, int fr, int fq) const {
;         const int row0 = u.pm * BM + wr * 64 + fr, col0 = u.pn * BM + wc * 32 + 4 * fq;
; #pragma unroll
;         for (int ai = 0; ai < 2; ++ai)
; #pragma unroll
;             for (int m = 0; m < 4; ++m) { const int row = row0 + ai * HALF + m * 16; const size_t ro = (size_t)row * 2048 + col0;
;                 float s = 0.f;
; #pragma unroll
;                 for (int bj = 0; bj < 2; ++bj)
; #pragma unroll
;                     for (int n = 0; n < 2; ++n) { f32x4 r;
;                         if (R32) r = *(const f32x4*)(R32 + ro + bj * HALF + n * 16);
;                         else { typedef unsigned u32x2_t __attribute__((ext_vector_type(2))); const u32x2_t rw = *(const u32x2_t*)(R16 + ro + bj * HALF + n * 16); const unsigned r0 = rw.x, r1 = rw.y;
;                             r = (f32x4){__builtin_bit_cast(float, r0 << 16), __builtin_bit_cast(float, r0 & 0xffff0000u), __builtin_bit_cast(float, r1 << 16), __builtin_bit_cast(float, r1 & 0xffff0000u)}; }
;                         const f32x4 v = acc[ai][bj][m][n] + r;
;                         typedef unsigned u32x2_s __attribute__((ext_vector_type(2))); u32x2_s w; w.x = cvt_pk_bf16(v[0], v[1]); w.y = cvt_pk_bf16(v[2], v[3]);
;                         *(u32x2_s*)(XB + ro + bj * HALF + n * 16) = w;
;                         s += (v[0] * v[0] + v[1] * v[1]) + (v[2] * v[2] + v[3] * v[3]); }
;                 s += __shfl_xor(s, 16); s += __shfl_xor(s, 32);
;                 if (fq == 0) ss2[(size_t)(u.pn * 4 + wc) * MT + row] = s; }
.LBB0_766:
	s_andn2_b64 vcc, exec, s[2:3]
	v_lshl_add_u64 v[102:103], v[106:107], 1, s[48:49]
	s_cbranch_vccnz .LBB0_768
	s_mov_b32 s100, 0x90000
	s_mov_b32 s101, 0
	v_lshl_add_u64 v[202:203], v[204:205], 0, s[100:101]
	global_load_dwordx2 v[164:165], v[202:203], off
	global_load_dwordx2 v[166:167], v[202:203], off offset:32
	global_load_dwordx2 v[168:169], v[202:203], off offset:256
	global_load_dwordx2 v[170:171], v[202:203], off offset:288
	s_waitcnt vmcnt(20)
	v_lshlrev_b32_e32 v96, 16, v172
	v_and_b32_e32 v97, 0xffff0000, v172
	v_lshlrev_b32_e32 v98, 16, v173
	v_and_b32_e32 v99, 0xffff0000, v173
.LBB0_768:
	v_pk_add_f32 v[98:99], v[94:95], v[98:99]
	v_pk_add_f32 v[104:105], v[92:93], v[96:97]
	v_lshl_add_u64 v[96:97], v[106:107], 1, s[90:91]
	v_cvt_pk_bf16_f32 v92, v104, v105
	v_cvt_pk_bf16_f32 v93, v98, v99
	s_and_b64 vcc, exec, s[40:41]
	s_mov_b64 s[2:3], -1
	global_store_dwordx2 v[96:97], v[92:93], off
	s_cbranch_vccnz .LBB0_770
	global_load_dwordx4 v[92:95], v[100:101], off offset:64
	s_waitcnt vmcnt(0)
	s_mov_b64 s[2:3], 0
.LBB0_770:
	s_andn2_b64 vcc, exec, s[2:3]
	s_cbranch_vccnz .LBB0_772
	v_lshlrev_b32_e32 v92, 16, v174
	v_and_b32_e32 v93, 0xffff0000, v174
	v_lshlrev_b32_e32 v94, 16, v175
	v_and_b32_e32 v95, 0xffff0000, v175
.LBB0_772:
	v_pk_add_f32 v[94:95], v[90:91], v[94:95]
	v_pk_add_f32 v[92:93], v[88:89], v[92:93]
	s_and_b64 vcc, exec, s[40:41]
	v_cvt_pk_bf16_f32 v88, v92, v93
	v_cvt_pk_bf16_f32 v89, v94, v95
	s_mov_b64 s[2:3], -1
	global_store_dwordx2 v[96:97], v[88:89], off offset:32
	s_cbranch_vccnz .LBB0_774
	global_load_dwordx4 v[88:91], v[100:101], off offset:512
	s_waitcnt vmcnt(0)
	s_mov_b64 s[2:3], 0
.LBB0_774:
	s_andn2_b64 vcc, exec, s[2:3]
	s_cbranch_vccnz .LBB0_776
	v_lshlrev_b32_e32 v88, 16, v176
	v_and_b32_e32 v89, 0xffff0000, v176
	v_lshlrev_b32_e32 v90, 16, v177
	v_and_b32_e32 v91, 0xffff0000, v177
.LBB0_776:
	v_pk_add_f32 v[90:91], v[86:87], v[90:91]
	v_pk_add_f32 v[88:89], v[84:85], v[88:89]
	s_and_b64 vcc, exec, s[40:41]
	v_cvt_pk_bf16_f32 v84, v88, v89
	v_cvt_pk_bf16_f32 v85, v90, v91
	s_mov_b64 s[2:3], -1
	global_store_dwordx2 v[96:97], v[84:85], off offset:256
	s_cbranch_vccnz .LBB0_778
	global_load_dwordx4 v[84:87], v[100:101], off offset:576
	s_waitcnt vmcnt(0)
	s_mov_b64 s[2:3], 0
.LBB0_778:
	s_andn2_b64 vcc, exec, s[2:3]
	s_cbranch_vccnz .LBB0_780
	v_lshlrev_b32_e32 v84, 16, v178
	v_and_b32_e32 v85, 0xffff0000, v178
	v_lshlrev_b32_e32 v86, 16, v179
	v_and_b32_e32 v87, 0xffff0000, v179
.LBB0_780:
	v_mul_f32_e32 v93, v93, v93
	v_mul_f32_e32 v100, v105, v105
	v_mul_f32_e32 v99, v99, v99
	v_fmac_f32_e32 v93, v92, v92
	v_mul_f32_e32 v92, v95, v95
	v_mul_f32_e32 v89, v89, v89
	v_fmac_f32_e32 v100, v104, v104
	v_fmac_f32_e32 v99, v98, v98
	v_fmac_f32_e32 v92, v94, v94
	v_fmac_f32_e32 v89, v88, v88
	v_mul_f32_e32 v88, v91, v91
	v_pk_add_f32 v[82:83], v[82:83], v[86:87]
	v_pk_add_f32 v[84:85], v[80:81], v[84:85]
	v_add_f32_e32 v98, v100, v99
	v_add_f32_e32 v92, v93, v92
	v_fmac_f32_e32 v88, v90, v90
	v_mul_f32_e32 v80, v85, v85
	v_mul_f32_e32 v81, v83, v83
	v_add_f32_e32 v92, v98, v92
	v_add_f32_e32 v88, v89, v88
	v_fmac_f32_e32 v80, v84, v84
	v_fmac_f32_e32 v81, v82, v82
	v_add_f32_e32 v88, v92, v88
	v_add_f32_e32 v80, v80, v81
	v_add_f32_e32 v80, v88, v80
	ds_bpermute_b32 v81, v150, v80
	v_cvt_pk_bf16_f32 v84, v84, v85
	v_cvt_pk_bf16_f32 v85, v82, v83
	global_store_dwordx2 v[96:97], v[84:85], off offset:288
	s_waitcnt lgkmcnt(0)
	v_add_f32_e32 v80, v80, v81
	ds_bpermute_b32 v81, v151, v80
	s_and_saveexec_b64 s[2:3], s[36:37]
	s_cbranch_execz .LBB0_782
	v_readlane_b32 s4, v250, 32
	v_readlane_b32 s5, v250, 33
	s_add_u32 s4, s4, s24
	s_addc_u32 s5, s5, s25
	v_lshl_add_u64 v[82:83], v[138:139], 2, s[4:5]
	s_waitcnt lgkmcnt(0)
	v_add_f32_e32 v80, v80, v81
	global_store_dword v[82:83], v80, off offset:128
.LBB0_782:
	s_or_b64 exec, exec, s[2:3]
	v_or_b32_e32 v80, 48, v138
	s_waitcnt lgkmcnt(0)
	v_ashrrev_i32_e32 v81, 31, v80
	v_lshlrev_b64 v[80:81], 11, v[80:81]
	v_readlane_b32 s4, v252, 2
	v_lshl_add_u64 v[90:91], v[80:81], 0, v[142:143]
	v_readlane_b32 s5, v252, 3
	s_mov_b64 s[2:3], -1
	s_and_b64 vcc, exec, s[40:41]
	v_lshl_add_u64 v[84:85], v[90:91], 2, s[4:5]
	v_readlane_b32 s6, v252, 4
	v_readlane_b32 s7, v252, 5
	v_readlane_b32 s8, v252, 6
	v_readlane_b32 s9, v252, 7
	v_readlane_b32 s10, v252, 8
	v_readlane_b32 s11, v252, 9
	v_readlane_b32 s12, v252, 10
	v_readlane_b32 s13, v252, 11
	v_readlane_b32 s14, v252, 12
	v_readlane_b32 s15, v252, 13
	v_readlane_b32 s16, v252, 14
	v_readlane_b32 s17, v252, 15
	v_readlane_b32 s18, v252, 16
	v_readlane_b32 s19, v252, 17
	s_cbranch_vccnz .LBB0_784
	global_load_dwordx4 v[80:83], v[84:85], off
	s_waitcnt vmcnt(0)
	s_mov_b64 s[2:3], 0
.LBB0_784:
	s_andn2_b64 vcc, exec, s[2:3]
	v_lshl_add_u64 v[86:87], v[90:91], 1, s[48:49]
	s_cbranch_vccnz .LBB0_786
	s_mov_b32 s100, 0xa0000
	s_mov_b32 s101, 0
	v_lshl_add_u64 v[202:203], v[204:205], 0, s[100:101]
	global_load_dwordx2 v[172:173], v[202:203], off
	global_load_dwordx2 v[174:175], v[202:203], off offset:32
	global_load_dwordx2 v[176:177], v[202:203], off offset:256
	global_load_dwordx2 v[178:179], v[202:203], off offset:288
	s_waitcnt vmcnt(24)
	v_lshlrev_b32_e32 v80, 16, v194
	v_and_b32_e32 v81, 0xffff0000, v194
	v_lshlrev_b32_e32 v82, 16, v195
	v_and_b32_e32 v83, 0xffff0000, v195
.LBB0_786:
	v_pk_add_f32 v[82:83], v[78:79], v[82:83]
	v_pk_add_f32 v[88:89], v[76:77], v[80:81]
	v_lshl_add_u64 v[80:81], v[90:91], 1, s[90:91]
	v_cvt_pk_bf16_f32 v76, v88, v89
	v_cvt_pk_bf16_f32 v77, v82, v83
	s_and_b64 vcc, exec, s[40:41]
	s_mov_b64 s[2:3], -1
	global_store_dwordx2 v[80:81], v[76:77], off
	s_cbranch_vccnz .LBB0_788
	global_load_dwordx4 v[76:79], v[84:85], off offset:64
	s_waitcnt vmcnt(0)
	s_mov_b64 s[2:3], 0
; __device__ __forceinline__ unsigned cvt_pk_bf16(float lo, float hi) { unsigned r; asm volatile("v_cvt_pk_bf16_f32 %0, %1, %2" : "=v"(r) : "v"(lo), "v"(hi)); return r; }
;     __device__ __forceinline__ void operator()(const f32x4 (&acc)[2][2][4][2], const Unit& u, int wr, int wc, int fr, int fq) const {
;     ...
;             for (int m = 0; m < 4; ++m) { const int row = row0 + ai * HALF + m * 16; const size_t ro = (size_t)row * 2048 + col0;
;                 float s = 0.f;
; #pragma unroll
;                 for (int bj = 0; bj < 2; ++bj)
; #pragma unroll
;                     for (int n = 0; n < 2; ++n) { f32x4 r;
;                         if (R32) r = *(const f32x4*)(R32 + ro + bj * HALF + n * 16);
;                         else { typedef unsigned u32x2_t __attribute__((ext_vector_type(2))); const u32x2_t rw = *(const u32x2_t*)(R16 + ro + bj * HALF + n * 16); const unsigned r0 = rw.x, r1 = rw.y;
;                             r = (f32x4){__builtin_bit_cast(float, r0 << 16), __builtin_bit_cast(float, r0 & 0xffff0000u), __builtin_bit_cast(float, r1 << 16), __builtin_bit_cast(float, r1 & 0xffff0000u)}; }
;                         const f32x4 v = acc[ai][bj][m][n] + r;
;                         typedef unsigned u32x2_s __attribute__((ext_vector_type(2))); u32x2_s w; w.x = cvt_pk_bf16(v[0], v[1]); w.y = cvt_pk_bf16(v[2], v[3]);
;                         *(u32x2_s*)(XB + ro + bj * HALF + n * 16) = w;
;                         s += (v[0] * v[0] + v[1] * v[1]) + (v[2] * v[2] + v[3] * v[3]); }
;                 s += __shfl_xor(s, 16); s += __shfl_xor(s, 32);
;                 if (fq == 0) ss2[(size_t)(u.pn * 4 + wc) * MT + row] = s; }
.LBB0_788:
	s_andn2_b64 vcc, exec, s[2:3]
	s_cbranch_vccnz .LBB0_790
	v_lshlrev_b32_e32 v76, 16, v196
	v_and_b32_e32 v77, 0xffff0000, v196
	v_lshlrev_b32_e32 v78, 16, v197
	v_and_b32_e32 v79, 0xffff0000, v197
.LBB0_790:
	v_pk_add_f32 v[78:79], v[74:75], v[78:79]
	v_pk_add_f32 v[76:77], v[72:73], v[76:77]
	s_and_b64 vcc, exec, s[40:41]
	v_cvt_pk_bf16_f32 v72, v76, v77
	v_cvt_pk_bf16_f32 v73, v78, v79
	s_mov_b64 s[2:3], -1
	global_store_dwordx2 v[80:81], v[72:73], off offset:32
	s_cbranch_vccnz .LBB0_792
	global_load_dwordx4 v[72:75], v[84:85], off offset:512
	s_waitcnt vmcnt(0)
	s_mov_b64 s[2:3], 0
.LBB0_792:
	s_andn2_b64 vcc, exec, s[2:3]
	s_cbranch_vccnz .LBB0_794
	v_lshlrev_b32_e32 v72, 16, v198
	v_and_b32_e32 v73, 0xffff0000, v198
	v_lshlrev_b32_e32 v74, 16, v199
	v_and_b32_e32 v75, 0xffff0000, v199
.LBB0_794:
	v_pk_add_f32 v[74:75], v[70:71], v[74:75]
	v_pk_add_f32 v[72:73], v[68:69], v[72:73]
	s_and_b64 vcc, exec, s[40:41]
	v_cvt_pk_bf16_f32 v68, v72, v73
	v_cvt_pk_bf16_f32 v69, v74, v75
	s_mov_b64 s[2:3], -1
	global_store_dwordx2 v[80:81], v[68:69], off offset:256
	s_cbranch_vccnz .LBB0_796
	global_load_dwordx4 v[68:71], v[84:85], off offset:576
	s_waitcnt vmcnt(0)
	s_mov_b64 s[2:3], 0
.LBB0_796:
	s_andn2_b64 vcc, exec, s[2:3]
	s_cbranch_vccnz .LBB0_798
	v_lshlrev_b32_e32 v68, 16, v200
	v_and_b32_e32 v69, 0xffff0000, v200
	v_lshlrev_b32_e32 v70, 16, v201
	v_and_b32_e32 v71, 0xffff0000, v201
.LBB0_798:
	v_mul_f32_e32 v77, v77, v77
	v_mul_f32_e32 v84, v89, v89
	v_mul_f32_e32 v83, v83, v83
	v_fmac_f32_e32 v77, v76, v76
	v_mul_f32_e32 v76, v79, v79
	v_mul_f32_e32 v73, v73, v73
	v_fmac_f32_e32 v84, v88, v88
	v_fmac_f32_e32 v83, v82, v82
	v_fmac_f32_e32 v76, v78, v78
	v_fmac_f32_e32 v73, v72, v72
	v_mul_f32_e32 v72, v75, v75
	v_pk_add_f32 v[66:67], v[66:67], v[70:71]
	v_pk_add_f32 v[68:69], v[64:65], v[68:69]
	v_add_f32_e32 v82, v84, v83
	v_add_f32_e32 v76, v77, v76
	v_fmac_f32_e32 v72, v74, v74
	v_mul_f32_e32 v64, v69, v69
	v_mul_f32_e32 v65, v67, v67
	v_add_f32_e32 v76, v82, v76
	v_add_f32_e32 v72, v73, v72
	v_fmac_f32_e32 v64, v68, v68
	v_fmac_f32_e32 v65, v66, v66
	v_add_f32_e32 v72, v76, v72
	v_add_f32_e32 v64, v64, v65
	v_add_f32_e32 v64, v72, v64
	ds_bpermute_b32 v65, v150, v64
	v_cvt_pk_bf16_f32 v68, v68, v69
	v_cvt_pk_bf16_f32 v69, v66, v67
	global_store_dwordx2 v[80:81], v[68:69], off offset:288
	s_waitcnt lgkmcnt(0)
	v_add_f32_e32 v64, v64, v65
	ds_bpermute_b32 v65, v151, v64
	s_and_saveexec_b64 s[2:3], s[36:37]
	s_cbranch_execz .LBB0_800
	v_readlane_b32 s4, v250, 32
	v_readlane_b32 s5, v250, 33
	s_add_u32 s4, s4, s24
	s_addc_u32 s5, s5, s25
	v_lshl_add_u64 v[66:67], v[138:139], 2, s[4:5]
	s_waitcnt lgkmcnt(0)
	v_add_f32_e32 v64, v64, v65
	global_store_dword v[66:67], v64, off offset:192
.LBB0_800:
	s_or_b64 exec, exec, s[2:3]
	s_mov_b64 s[2:3], 0x40000
	v_readlane_b32 s4, v252, 2
	v_lshl_add_u64 v[74:75], v[140:141], 0, s[2:3]
	v_readlane_b32 s5, v252, 3
	s_mov_b64 s[2:3], -1
	s_and_b64 vcc, exec, s[40:41]
	v_lshl_add_u64 v[68:69], v[74:75], 2, s[4:5]
	v_readlane_b32 s6, v252, 4
	v_readlane_b32 s7, v252, 5
	v_readlane_b32 s8, v252, 6
	v_readlane_b32 s9, v252, 7
	v_readlane_b32 s10, v252, 8
	v_readlane_b32 s11, v252, 9
	v_readlane_b32 s12, v252, 10
	v_readlane_b32 s13, v252, 11
	v_readlane_b32 s14, v252, 12
	v_readlane_b32 s15, v252, 13
	v_readlane_b32 s16, v252, 14
	v_readlane_b32 s17, v252, 15
	v_readlane_b32 s18, v252, 16
	v_readlane_b32 s19, v252, 17
	s_cbranch_vccnz .LBB0_802
	s_waitcnt lgkmcnt(0)
	global_load_dwordx4 v[64:67], v[68:69], off
	s_waitcnt vmcnt(0)
	s_mov_b64 s[2:3], 0
.LBB0_802:
	s_andn2_b64 vcc, exec, s[2:3]
	v_lshl_add_u64 v[70:71], v[74:75], 1, s[48:49]
	s_cbranch_vccnz .LBB0_804
	s_mov_b32 s100, 0xb0000
	s_mov_b32 s101, 0
	v_lshl_add_u64 v[202:203], v[204:205], 0, s[100:101]
	global_load_dwordx2 v[194:195], v[202:203], off
	global_load_dwordx2 v[196:197], v[202:203], off offset:32
	global_load_dwordx2 v[198:199], v[202:203], off offset:256
	global_load_dwordx2 v[200:201], v[202:203], off offset:288
	s_waitcnt vmcnt(24)
	v_lshlrev_b32_e32 v64, 16, v156
	s_waitcnt lgkmcnt(0)
	v_and_b32_e32 v65, 0xffff0000, v156
	v_lshlrev_b32_e32 v66, 16, v157
	v_and_b32_e32 v67, 0xffff0000, v157
.LBB0_804:
	v_pk_add_f32 v[66:67], v[62:63], v[66:67]
	s_waitcnt lgkmcnt(0)
	v_pk_add_f32 v[72:73], v[60:61], v[64:65]
	v_lshl_add_u64 v[64:65], v[74:75], 1, s[90:91]
	v_cvt_pk_bf16_f32 v60, v72, v73
	v_cvt_pk_bf16_f32 v61, v66, v67
	s_and_b64 vcc, exec, s[40:41]
	s_mov_b64 s[2:3], -1
	global_store_dwordx2 v[64:65], v[60:61], off
	s_cbranch_vccnz .LBB0_806
	global_load_dwordx4 v[60:63], v[68:69], off offset:64
	s_waitcnt vmcnt(0)
	s_mov_b64 s[2:3], 0
.LBB0_806:
	s_andn2_b64 vcc, exec, s[2:3]
	s_cbranch_vccnz .LBB0_808
	v_lshlrev_b32_e32 v60, 16, v158
	v_and_b32_e32 v61, 0xffff0000, v158
	v_lshlrev_b32_e32 v62, 16, v159
	v_and_b32_e32 v63, 0xffff0000, v159
.LBB0_808:
	v_pk_add_f32 v[62:63], v[58:59], v[62:63]
	v_pk_add_f32 v[60:61], v[56:57], v[60:61]
	s_and_b64 vcc, exec, s[40:41]
	v_cvt_pk_bf16_f32 v56, v60, v61
	v_cvt_pk_bf16_f32 v57, v62, v63
	s_mov_b64 s[2:3], -1
	global_store_dwordx2 v[64:65], v[56:57], off offset:32
	s_cbranch_vccnz .LBB0_810
	global_load_dwordx4 v[56:59], v[68:69], off offset:512
	s_waitcnt vmcnt(0)
	s_mov_b64 s[2:3], 0
.LBB0_810:
	s_andn2_b64 vcc, exec, s[2:3]
	s_cbranch_vccnz .LBB0_812
	v_lshlrev_b32_e32 v56, 16, v160
	v_and_b32_e32 v57, 0xffff0000, v160
	v_lshlrev_b32_e32 v58, 16, v161
	v_and_b32_e32 v59, 0xffff0000, v161
; __device__ __forceinline__ unsigned cvt_pk_bf16(float lo, float hi) { unsigned r; asm volatile("v_cvt_pk_bf16_f32 %0, %1, %2" : "=v"(r) : "v"(lo), "v"(hi)); return r; }
;     __device__ __forceinline__ void operator()(const f32x4 (&acc)[2][2][4][2], const Unit& u, int wr, int wc, int fr, int fq) const {
;     ...
;             for (int m = 0; m < 4; ++m) { const int row = row0 + ai * HALF + m * 16; const size_t ro = (size_t)row * 2048 + col0;
;                 float s = 0.f;
; #pragma unroll
;                 for (int bj = 0; bj < 2; ++bj)
; #pragma unroll
;                     for (int n = 0; n < 2; ++n) { f32x4 r;
;                         if (R32) r = *(const f32x4*)(R32 + ro + bj * HALF + n * 16);
;                         else { typedef unsigned u32x2_t __attribute__((ext_vector_type(2))); const u32x2_t rw = *(const u32x2_t*)(R16 + ro + bj * HALF + n * 16); const unsigned r0 = rw.x, r1 = rw.y;
;                             r = (f32x4){__builtin_bit_cast(float, r0 << 16), __builtin_bit_cast(float, r0 & 0xffff0000u), __builtin_bit_cast(float, r1 << 16), __builtin_bit_cast(float, r1 & 0xffff0000u)}; }
;                         const f32x4 v = acc[ai][bj][m][n] + r;
;                         typedef unsigned u32x2_s __attribute__((ext_vector_type(2))); u32x2_s w; w.x = cvt_pk_bf16(v[0], v[1]); w.y = cvt_pk_bf16(v[2], v[3]);
;                         *(u32x2_s*)(XB + ro + bj * HALF + n * 16) = w;
;                         s += (v[0] * v[0] + v[1] * v[1]) + (v[2] * v[2] + v[3] * v[3]); }
;                 s += __shfl_xor(s, 16); s += __shfl_xor(s, 32);
;                 if (fq == 0) ss2[(size_t)(u.pn * 4 + wc) * MT + row] = s; }
.LBB0_812:
	v_pk_add_f32 v[58:59], v[54:55], v[58:59]
	v_pk_add_f32 v[56:57], v[52:53], v[56:57]
	s_and_b64 vcc, exec, s[40:41]
	v_cvt_pk_bf16_f32 v52, v56, v57
	v_cvt_pk_bf16_f32 v53, v58, v59
	s_mov_b64 s[2:3], -1
	global_store_dwordx2 v[64:65], v[52:53], off offset:256
	s_cbranch_vccnz .LBB0_814
	global_load_dwordx4 v[52:55], v[68:69], off offset:576
	s_waitcnt vmcnt(0)
	s_mov_b64 s[2:3], 0
.LBB0_814:
	s_andn2_b64 vcc, exec, s[2:3]
	s_cbranch_vccnz .LBB0_816
	v_lshlrev_b32_e32 v52, 16, v162
	v_and_b32_e32 v53, 0xffff0000, v162
	v_lshlrev_b32_e32 v54, 16, v163
	v_and_b32_e32 v55, 0xffff0000, v163
.LBB0_816:
	v_mul_f32_e32 v61, v61, v61
	v_mul_f32_e32 v68, v73, v73
	v_mul_f32_e32 v67, v67, v67
	v_fmac_f32_e32 v61, v60, v60
	v_mul_f32_e32 v60, v63, v63
	v_mul_f32_e32 v57, v57, v57
	v_fmac_f32_e32 v68, v72, v72
	v_fmac_f32_e32 v67, v66, v66
	v_fmac_f32_e32 v60, v62, v62
	v_fmac_f32_e32 v57, v56, v56
	v_mul_f32_e32 v56, v59, v59
	v_pk_add_f32 v[50:51], v[50:51], v[54:55]
	v_pk_add_f32 v[52:53], v[48:49], v[52:53]
	v_add_f32_e32 v66, v68, v67
	v_add_f32_e32 v60, v61, v60
	v_fmac_f32_e32 v56, v58, v58
	v_mul_f32_e32 v48, v53, v53
	v_mul_f32_e32 v49, v51, v51
	v_add_f32_e32 v60, v66, v60
	v_add_f32_e32 v56, v57, v56
	v_fmac_f32_e32 v48, v52, v52
	v_fmac_f32_e32 v49, v50, v50
	v_add_f32_e32 v56, v60, v56
	v_add_f32_e32 v48, v48, v49
	v_add_f32_e32 v48, v56, v48
	ds_bpermute_b32 v49, v150, v48
	v_cvt_pk_bf16_f32 v52, v52, v53
	v_cvt_pk_bf16_f32 v53, v50, v51
	global_store_dwordx2 v[64:65], v[52:53], off offset:288
	s_waitcnt lgkmcnt(0)
	v_add_f32_e32 v48, v48, v49
	ds_bpermute_b32 v49, v151, v48
	s_and_saveexec_b64 s[2:3], s[36:37]
	s_cbranch_execz .LBB0_818
	v_readlane_b32 s4, v250, 32
	v_readlane_b32 s5, v250, 33
	s_add_u32 s4, s4, s24
	s_addc_u32 s5, s5, s25
	v_lshl_add_u64 v[50:51], v[138:139], 2, s[4:5]
	s_waitcnt lgkmcnt(0)
	v_add_f32_e32 v48, v48, v49
	global_store_dword v[50:51], v48, off offset:512
.LBB0_818:
	s_or_b64 exec, exec, s[2:3]
	s_mov_b64 s[2:3], 0x48000
	v_readlane_b32 s4, v252, 2
	v_lshl_add_u64 v[58:59], v[140:141], 0, s[2:3]
	v_readlane_b32 s5, v252, 3
	s_mov_b64 s[2:3], -1
	s_and_b64 vcc, exec, s[40:41]
	v_lshl_add_u64 v[52:53], v[58:59], 2, s[4:5]
	v_readlane_b32 s6, v252, 4
	v_readlane_b32 s7, v252, 5
	v_readlane_b32 s8, v252, 6
	v_readlane_b32 s9, v252, 7
	v_readlane_b32 s10, v252, 8
	v_readlane_b32 s11, v252, 9
	v_readlane_b32 s12, v252, 10
	v_readlane_b32 s13, v252, 11
	v_readlane_b32 s14, v252, 12
	v_readlane_b32 s15, v252, 13
	v_readlane_b32 s16, v252, 14
	v_readlane_b32 s17, v252, 15
	v_readlane_b32 s18, v252, 16
	v_readlane_b32 s19, v252, 17
	s_cbranch_vccnz .LBB0_820
	s_waitcnt lgkmcnt(0)
	global_load_dwordx4 v[48:51], v[52:53], off
	s_waitcnt vmcnt(0)
	s_mov_b64 s[2:3], 0
.LBB0_820:
	s_andn2_b64 vcc, exec, s[2:3]
	v_lshl_add_u64 v[54:55], v[58:59], 1, s[48:49]
	s_cbranch_vccnz .LBB0_822
	s_waitcnt vmcnt(20)
	v_lshlrev_b32_e32 v48, 16, v164
	s_waitcnt lgkmcnt(0)
	v_and_b32_e32 v49, 0xffff0000, v164
	v_lshlrev_b32_e32 v50, 16, v165
	v_and_b32_e32 v51, 0xffff0000, v165
.LBB0_822:
	v_pk_add_f32 v[50:51], v[46:47], v[50:51]
	s_waitcnt lgkmcnt(0)
	v_pk_add_f32 v[56:57], v[44:45], v[48:49]
	v_lshl_add_u64 v[48:49], v[58:59], 1, s[90:91]
	v_cvt_pk_bf16_f32 v44, v56, v57
	v_cvt_pk_bf16_f32 v45, v50, v51
	s_and_b64 vcc, exec, s[40:41]
	s_mov_b64 s[2:3], -1
	global_store_dwordx2 v[48:49], v[44:45], off
	s_cbranch_vccnz .LBB0_824
	global_load_dwordx4 v[44:47], v[52:53], off offset:64
	s_waitcnt vmcnt(0)
	s_mov_b64 s[2:3], 0
.LBB0_824:
	s_andn2_b64 vcc, exec, s[2:3]
	s_cbranch_vccnz .LBB0_826
	v_lshlrev_b32_e32 v44, 16, v166
	v_and_b32_e32 v45, 0xffff0000, v166
	v_lshlrev_b32_e32 v46, 16, v167
	v_and_b32_e32 v47, 0xffff0000, v167
.LBB0_826:
	v_pk_add_f32 v[46:47], v[42:43], v[46:47]
	v_pk_add_f32 v[44:45], v[40:41], v[44:45]
	s_and_b64 vcc, exec, s[40:41]
	v_cvt_pk_bf16_f32 v40, v44, v45
	v_cvt_pk_bf16_f32 v41, v46, v47
	s_mov_b64 s[2:3], -1
	global_store_dwordx2 v[48:49], v[40:41], off offset:32
	s_cbranch_vccnz .LBB0_828
	global_load_dwordx4 v[40:43], v[52:53], off offset:512
	s_waitcnt vmcnt(0)
	s_mov_b64 s[2:3], 0
.LBB0_828:
	s_andn2_b64 vcc, exec, s[2:3]
	s_cbranch_vccnz .LBB0_830
	v_lshlrev_b32_e32 v40, 16, v168
	v_and_b32_e32 v41, 0xffff0000, v168
	v_lshlrev_b32_e32 v42, 16, v169
	v_and_b32_e32 v43, 0xffff0000, v169
.LBB0_830:
	v_pk_add_f32 v[42:43], v[38:39], v[42:43]
	v_pk_add_f32 v[40:41], v[36:37], v[40:41]
	s_and_b64 vcc, exec, s[40:41]
	v_cvt_pk_bf16_f32 v36, v40, v41
	v_cvt_pk_bf16_f32 v37, v42, v43
	s_mov_b64 s[2:3], -1
	global_store_dwordx2 v[48:49], v[36:37], off offset:256
	s_cbranch_vccnz .LBB0_832
	global_load_dwordx4 v[36:39], v[52:53], off offset:576
	s_waitcnt vmcnt(0)
	s_mov_b64 s[2:3], 0
.LBB0_832:
	s_andn2_b64 vcc, exec, s[2:3]
	s_cbranch_vccnz .LBB0_834
	v_lshlrev_b32_e32 v36, 16, v170
	v_and_b32_e32 v37, 0xffff0000, v170
	v_lshlrev_b32_e32 v38, 16, v171
	v_and_b32_e32 v39, 0xffff0000, v171
.LBB0_834:
	v_mul_f32_e32 v45, v45, v45
	v_mul_f32_e32 v52, v57, v57
	v_mul_f32_e32 v51, v51, v51
	v_fmac_f32_e32 v45, v44, v44
	v_mul_f32_e32 v44, v47, v47
	v_mul_f32_e32 v41, v41, v41
	v_fmac_f32_e32 v52, v56, v56
	v_fmac_f32_e32 v51, v50, v50
	v_fmac_f32_e32 v44, v46, v46
	v_fmac_f32_e32 v41, v40, v40
	v_mul_f32_e32 v40, v43, v43
	v_pk_add_f32 v[34:35], v[34:35], v[38:39]
	v_pk_add_f32 v[36:37], v[32:33], v[36:37]
	v_add_f32_e32 v50, v52, v51
	v_add_f32_e32 v44, v45, v44
	v_fmac_f32_e32 v40, v42, v42
	v_mul_f32_e32 v32, v37, v37
	v_mul_f32_e32 v33, v35, v35
	v_add_f32_e32 v44, v50, v44
	v_add_f32_e32 v40, v41, v40
	v_fmac_f32_e32 v32, v36, v36
	v_fmac_f32_e32 v33, v34, v34
	v_add_f32_e32 v40, v44, v40
	v_add_f32_e32 v32, v32, v33
	v_add_f32_e32 v32, v40, v32
	ds_bpermute_b32 v33, v150, v32
	v_cvt_pk_bf16_f32 v36, v36, v37
	v_cvt_pk_bf16_f32 v37, v34, v35
	global_store_dwordx2 v[48:49], v[36:37], off offset:288
	s_waitcnt lgkmcnt(0)
	v_add_f32_e32 v32, v32, v33
	ds_bpermute_b32 v33, v151, v32
	s_and_saveexec_b64 s[2:3], s[36:37]
	s_cbranch_execz .LBB0_836
	v_readlane_b32 s4, v250, 32
	v_readlane_b32 s5, v250, 33
	s_add_u32 s4, s4, s24
	s_addc_u32 s5, s5, s25
	v_lshl_add_u64 v[34:35], v[138:139], 2, s[4:5]
	s_waitcnt lgkmcnt(0)
	v_add_f32_e32 v32, v32, v33
	global_store_dword v[34:35], v32, off offset:576
; __device__ __forceinline__ unsigned cvt_pk_bf16(float lo, float hi) { unsigned r; asm volatile("v_cvt_pk_bf16_f32 %0, %1, %2" : "=v"(r) : "v"(lo), "v"(hi)); return r; }
;     __device__ __forceinline__ void operator()(const f32x4 (&acc)[2][2][4][2], const Unit& u, int wr, int wc, int fr, int fq) const {
;     ...
;             for (int m = 0; m < 4; ++m) { const int row = row0 + ai * HALF + m * 16; const size_t ro = (size_t)row * 2048 + col0;
;                 float s = 0.f;
; #pragma unroll
;                 for (int bj = 0; bj < 2; ++bj)
; #pragma unroll
;                     for (int n = 0; n < 2; ++n) { f32x4 r;
;                         if (R32) r = *(const f32x4*)(R32 + ro + bj * HALF + n * 16);
;                         else { typedef unsigned u32x2_t __attribute__((ext_vector_type(2))); const u32x2_t rw = *(const u32x2_t*)(R16 + ro + bj * HALF + n * 16); const unsigned r0 = rw.x, r1 = rw.y;
;                             r = (f32x4){__builtin_bit_cast(float, r0 << 16), __builtin_bit_cast(float, r0 & 0xffff0000u), __builtin_bit_cast(float, r1 << 16), __builtin_bit_cast(float, r1 & 0xffff0000u)}; }
;                         const f32x4 v = acc[ai][bj][m][n] + r;
;                         typedef unsigned u32x2_s __attribute__((ext_vector_type(2))); u32x2_s w; w.x = cvt_pk_bf16(v[0], v[1]); w.y = cvt_pk_bf16(v[2], v[3]);
;                         *(u32x2_s*)(XB + ro + bj * HALF + n * 16) = w;
;                         s += (v[0] * v[0] + v[1] * v[1]) + (v[2] * v[2] + v[3] * v[3]); }
;                 s += __shfl_xor(s, 16); s += __shfl_xor(s, 32);
;                 if (fq == 0) ss2[(size_t)(u.pn * 4 + wc) * MT + row] = s; }
.LBB0_836:
	s_or_b64 exec, exec, s[2:3]
	s_mov_b64 s[2:3], 0x50000
	v_readlane_b32 s4, v252, 2
	v_lshl_add_u64 v[42:43], v[140:141], 0, s[2:3]
	v_readlane_b32 s5, v252, 3
	s_mov_b64 s[2:3], -1
	s_and_b64 vcc, exec, s[40:41]
	v_lshl_add_u64 v[36:37], v[42:43], 2, s[4:5]
	v_readlane_b32 s6, v252, 4
	v_readlane_b32 s7, v252, 5
	v_readlane_b32 s8, v252, 6
	v_readlane_b32 s9, v252, 7
	v_readlane_b32 s10, v252, 8
	v_readlane_b32 s11, v252, 9
	v_readlane_b32 s12, v252, 10
	v_readlane_b32 s13, v252, 11
	v_readlane_b32 s14, v252, 12
	v_readlane_b32 s15, v252, 13
	v_readlane_b32 s16, v252, 14
	v_readlane_b32 s17, v252, 15
	v_readlane_b32 s18, v252, 16
	v_readlane_b32 s19, v252, 17
	s_cbranch_vccnz .LBB0_838
	s_waitcnt lgkmcnt(0)
	global_load_dwordx4 v[32:35], v[36:37], off
	s_waitcnt vmcnt(0)
	s_mov_b64 s[2:3], 0
.LBB0_838:
	s_andn2_b64 vcc, exec, s[2:3]
	v_lshl_add_u64 v[38:39], v[42:43], 1, s[48:49]
	s_cbranch_vccnz .LBB0_840
	s_waitcnt vmcnt(16)
	v_lshlrev_b32_e32 v32, 16, v172
	s_waitcnt lgkmcnt(0)
	v_and_b32_e32 v33, 0xffff0000, v172
	v_lshlrev_b32_e32 v34, 16, v173
	v_and_b32_e32 v35, 0xffff0000, v173
.LBB0_840:
	v_pk_add_f32 v[34:35], v[30:31], v[34:35]
	s_waitcnt lgkmcnt(0)
	v_pk_add_f32 v[40:41], v[28:29], v[32:33]
	v_lshl_add_u64 v[32:33], v[42:43], 1, s[90:91]
	v_cvt_pk_bf16_f32 v28, v40, v41
	v_cvt_pk_bf16_f32 v29, v34, v35
	s_and_b64 vcc, exec, s[40:41]
	s_mov_b64 s[2:3], -1
	global_store_dwordx2 v[32:33], v[28:29], off
	s_cbranch_vccnz .LBB0_842
	global_load_dwordx4 v[28:31], v[36:37], off offset:64
	s_waitcnt vmcnt(0)
	s_mov_b64 s[2:3], 0
.LBB0_842:
	s_andn2_b64 vcc, exec, s[2:3]
	s_cbranch_vccnz .LBB0_844
	v_lshlrev_b32_e32 v28, 16, v174
	v_and_b32_e32 v29, 0xffff0000, v174
	v_lshlrev_b32_e32 v30, 16, v175
	v_and_b32_e32 v31, 0xffff0000, v175
.LBB0_844:
	v_pk_add_f32 v[30:31], v[26:27], v[30:31]
	v_pk_add_f32 v[28:29], v[24:25], v[28:29]
	s_and_b64 vcc, exec, s[40:41]
	v_cvt_pk_bf16_f32 v24, v28, v29
	v_cvt_pk_bf16_f32 v25, v30, v31
	s_mov_b64 s[2:3], -1
	global_store_dwordx2 v[32:33], v[24:25], off offset:32
	s_cbranch_vccnz .LBB0_846
	global_load_dwordx4 v[24:27], v[36:37], off offset:512
	s_waitcnt vmcnt(0)
	s_mov_b64 s[2:3], 0
.LBB0_846:
	s_andn2_b64 vcc, exec, s[2:3]
	s_cbranch_vccnz .LBB0_848
	v_lshlrev_b32_e32 v24, 16, v176
	v_and_b32_e32 v25, 0xffff0000, v176
	v_lshlrev_b32_e32 v26, 16, v177
	v_and_b32_e32 v27, 0xffff0000, v177
.LBB0_848:
	v_pk_add_f32 v[26:27], v[22:23], v[26:27]
	v_pk_add_f32 v[24:25], v[20:21], v[24:25]
	s_and_b64 vcc, exec, s[40:41]
	v_cvt_pk_bf16_f32 v20, v24, v25
	v_cvt_pk_bf16_f32 v21, v26, v27
	s_mov_b64 s[2:3], -1
	global_store_dwordx2 v[32:33], v[20:21], off offset:256
	s_cbranch_vccnz .LBB0_850
	global_load_dwordx4 v[20:23], v[36:37], off offset:576
	s_waitcnt vmcnt(0)
	s_mov_b64 s[2:3], 0
.LBB0_850:
	s_andn2_b64 vcc, exec, s[2:3]
	s_cbranch_vccnz .LBB0_852
	v_lshlrev_b32_e32 v20, 16, v178
	v_and_b32_e32 v21, 0xffff0000, v178
	v_lshlrev_b32_e32 v22, 16, v179
	v_and_b32_e32 v23, 0xffff0000, v179
.LBB0_852:
	v_mul_f32_e32 v29, v29, v29
	v_mul_f32_e32 v36, v41, v41
	v_mul_f32_e32 v35, v35, v35
	v_fmac_f32_e32 v29, v28, v28
	v_mul_f32_e32 v28, v31, v31
	v_mul_f32_e32 v25, v25, v25
	v_fmac_f32_e32 v36, v40, v40
	v_fmac_f32_e32 v35, v34, v34
	v_fmac_f32_e32 v28, v30, v30
	v_fmac_f32_e32 v25, v24, v24
	v_mul_f32_e32 v24, v27, v27
	v_pk_add_f32 v[18:19], v[18:19], v[22:23]
	v_pk_add_f32 v[20:21], v[16:17], v[20:21]
	v_add_f32_e32 v34, v36, v35
	v_add_f32_e32 v28, v29, v28
	v_fmac_f32_e32 v24, v26, v26
	v_mul_f32_e32 v16, v21, v21
	v_mul_f32_e32 v17, v19, v19
	v_add_f32_e32 v28, v34, v28
	v_add_f32_e32 v24, v25, v24
	v_fmac_f32_e32 v16, v20, v20
	v_fmac_f32_e32 v17, v18, v18
	v_add_f32_e32 v24, v28, v24
	v_add_f32_e32 v16, v16, v17
	v_add_f32_e32 v16, v24, v16
	ds_bpermute_b32 v17, v150, v16
	v_cvt_pk_bf16_f32 v20, v20, v21
	v_cvt_pk_bf16_f32 v21, v18, v19
	global_store_dwordx2 v[32:33], v[20:21], off offset:288
	s_waitcnt lgkmcnt(0)
	v_add_f32_e32 v16, v16, v17
	ds_bpermute_b32 v17, v151, v16
	s_and_saveexec_b64 s[2:3], s[36:37]
	s_cbranch_execz .LBB0_854
	v_readlane_b32 s4, v250, 32
	v_readlane_b32 s5, v250, 33
	s_add_u32 s4, s4, s24
	s_addc_u32 s5, s5, s25
	v_lshl_add_u64 v[18:19], v[138:139], 2, s[4:5]
	s_waitcnt lgkmcnt(0)
	v_add_f32_e32 v16, v16, v17
	global_store_dword v[18:19], v16, off offset:640
; __device__ __forceinline__ unsigned cvt_pk_bf16(float lo, float hi) { unsigned r; asm volatile("v_cvt_pk_bf16_f32 %0, %1, %2" : "=v"(r) : "v"(lo), "v"(hi)); return r; }
;     __device__ __forceinline__ void operator()(const f32x4 (&acc)[2][2][4][2], const Unit& u, int wr, int wc, int fr, int fq) const {
;     ...
;             for (int m = 0; m < 4; ++m) { const int row = row0 + ai * HALF + m * 16; const size_t ro = (size_t)row * 2048 + col0;
;                 float s = 0.f;
; #pragma unroll
;                 for (int bj = 0; bj < 2; ++bj)
; #pragma unroll
;                     for (int n = 0; n < 2; ++n) { f32x4 r;
;                         if (R32) r = *(const f32x4*)(R32 + ro + bj * HALF + n * 16);
;                         else { typedef unsigned u32x2_t __attribute__((ext_vector_type(2))); const u32x2_t rw = *(const u32x2_t*)(R16 + ro + bj * HALF + n * 16); const unsigned r0 = rw.x, r1 = rw.y;
;                             r = (f32x4){__builtin_bit_cast(float, r0 << 16), __builtin_bit_cast(float, r0 & 0xffff0000u), __builtin_bit_cast(float, r1 << 16), __builtin_bit_cast(float, r1 & 0xffff0000u)}; }
;                         const f32x4 v = acc[ai][bj][m][n] + r;
;                         typedef unsigned u32x2_s __attribute__((ext_vector_type(2))); u32x2_s w; w.x = cvt_pk_bf16(v[0], v[1]); w.y = cvt_pk_bf16(v[2], v[3]);
;                         *(u32x2_s*)(XB + ro + bj * HALF + n * 16) = w;
;                         s += (v[0] * v[0] + v[1] * v[1]) + (v[2] * v[2] + v[3] * v[3]); }
;                 s += __shfl_xor(s, 16); s += __shfl_xor(s, 32);
;                 if (fq == 0) ss2[(size_t)(u.pn * 4 + wc) * MT + row] = s; }
.LBB0_854:
	s_or_b64 exec, exec, s[2:3]
	s_mov_b64 s[2:3], 0x58000
	v_readlane_b32 s4, v252, 2
	v_lshl_add_u64 v[26:27], v[140:141], 0, s[2:3]
	v_readlane_b32 s5, v252, 3
	s_mov_b64 s[2:3], -1
	s_and_b64 vcc, exec, s[40:41]
	v_lshl_add_u64 v[22:23], v[26:27], 2, s[4:5]
	v_readlane_b32 s6, v252, 4
	v_readlane_b32 s7, v252, 5
	v_readlane_b32 s8, v252, 6
	v_readlane_b32 s9, v252, 7
	v_readlane_b32 s10, v252, 8
	v_readlane_b32 s11, v252, 9
	v_readlane_b32 s12, v252, 10
	v_readlane_b32 s13, v252, 11
	v_readlane_b32 s14, v252, 12
	v_readlane_b32 s15, v252, 13
	v_readlane_b32 s16, v252, 14
	v_readlane_b32 s17, v252, 15
	v_readlane_b32 s18, v252, 16
	v_readlane_b32 s19, v252, 17
	s_cbranch_vccnz .LBB0_856
	s_waitcnt lgkmcnt(0)
	global_load_dwordx4 v[16:19], v[22:23], off
	s_waitcnt vmcnt(0)
	s_mov_b64 s[2:3], 0
.LBB0_856:
	s_andn2_b64 vcc, exec, s[2:3]
	v_lshl_add_u64 v[20:21], v[26:27], 1, s[48:49]
	s_cbranch_vccnz .LBB0_858
	s_waitcnt vmcnt(12)
	v_lshlrev_b32_e32 v16, 16, v194
	s_waitcnt lgkmcnt(0)
	v_and_b32_e32 v17, 0xffff0000, v194
	v_lshlrev_b32_e32 v18, 16, v195
	v_and_b32_e32 v19, 0xffff0000, v195
.LBB0_858:
	v_pk_add_f32 v[18:19], v[14:15], v[18:19]
	s_waitcnt lgkmcnt(0)
	v_pk_add_f32 v[24:25], v[12:13], v[16:17]
	v_lshl_add_u64 v[16:17], v[26:27], 1, s[90:91]
	v_cvt_pk_bf16_f32 v12, v24, v25
	v_cvt_pk_bf16_f32 v13, v18, v19
	s_and_b64 vcc, exec, s[40:41]
	s_mov_b64 s[2:3], -1
	global_store_dwordx2 v[16:17], v[12:13], off
	s_cbranch_vccnz .LBB0_860
	global_load_dwordx4 v[12:15], v[22:23], off offset:64
	s_waitcnt vmcnt(0)
	s_mov_b64 s[2:3], 0
.LBB0_860:
	s_andn2_b64 vcc, exec, s[2:3]
	s_cbranch_vccnz .LBB0_862
	v_lshlrev_b32_e32 v12, 16, v196
	v_and_b32_e32 v13, 0xffff0000, v196
	v_lshlrev_b32_e32 v14, 16, v197
	v_and_b32_e32 v15, 0xffff0000, v197
.LBB0_862:
	v_pk_add_f32 v[14:15], v[10:11], v[14:15]
	v_pk_add_f32 v[12:13], v[8:9], v[12:13]
	s_and_b64 vcc, exec, s[40:41]
	v_cvt_pk_bf16_f32 v8, v12, v13
	v_cvt_pk_bf16_f32 v9, v14, v15
	s_mov_b64 s[2:3], -1
	global_store_dwordx2 v[16:17], v[8:9], off offset:32
	s_cbranch_vccnz .LBB0_864
	global_load_dwordx4 v[8:11], v[22:23], off offset:512
	s_waitcnt vmcnt(0)
	s_mov_b64 s[2:3], 0
.LBB0_864:
	s_andn2_b64 vcc, exec, s[2:3]
	s_cbranch_vccnz .LBB0_866
	v_lshlrev_b32_e32 v8, 16, v198
	v_and_b32_e32 v9, 0xffff0000, v198
	v_lshlrev_b32_e32 v10, 16, v199
	v_and_b32_e32 v11, 0xffff0000, v199
.LBB0_866:
	v_pk_add_f32 v[10:11], v[6:7], v[10:11]
	v_pk_add_f32 v[8:9], v[4:5], v[8:9]
	s_and_b64 vcc, exec, s[40:41]
	v_cvt_pk_bf16_f32 v4, v8, v9
	v_cvt_pk_bf16_f32 v5, v10, v11
	s_mov_b64 s[2:3], -1
	global_store_dwordx2 v[16:17], v[4:5], off offset:256
	s_cbranch_vccnz .LBB0_868
	global_load_dwordx4 v[4:7], v[22:23], off offset:576
	s_waitcnt vmcnt(0)
	s_mov_b64 s[2:3], 0
.LBB0_868:
	v_readlane_b32 s6, v250, 32
	s_andn2_b64 vcc, exec, s[2:3]
	v_readlane_b32 s7, v250, 33
	s_cbranch_vccnz .LBB0_870
	v_lshlrev_b32_e32 v4, 16, v200
	v_and_b32_e32 v5, 0xffff0000, v200
	v_lshlrev_b32_e32 v6, 16, v201
	v_and_b32_e32 v7, 0xffff0000, v201
.LBB0_870:
	v_mul_f32_e32 v13, v13, v13
	v_mul_f32_e32 v20, v25, v25
	v_mul_f32_e32 v19, v19, v19
	v_fmac_f32_e32 v13, v12, v12
	v_mul_f32_e32 v12, v15, v15
	v_mul_f32_e32 v9, v9, v9
	v_fmac_f32_e32 v20, v24, v24
	v_fmac_f32_e32 v19, v18, v18
	v_fmac_f32_e32 v12, v14, v14
	v_fmac_f32_e32 v9, v8, v8
	v_mul_f32_e32 v8, v11, v11
	v_pk_add_f32 v[2:3], v[2:3], v[6:7]
	v_pk_add_f32 v[4:5], v[0:1], v[4:5]
	v_add_f32_e32 v18, v20, v19
	v_add_f32_e32 v12, v13, v12
	v_fmac_f32_e32 v8, v10, v10
	v_mul_f32_e32 v0, v5, v5
	v_mul_f32_e32 v1, v3, v3
	v_add_f32_e32 v12, v18, v12
	v_add_f32_e32 v8, v9, v8
	v_fmac_f32_e32 v0, v4, v4
	v_fmac_f32_e32 v1, v2, v2
	v_add_f32_e32 v8, v12, v8
	v_add_f32_e32 v0, v0, v1
	v_add_f32_e32 v0, v8, v0
	ds_bpermute_b32 v1, v150, v0
	v_cvt_pk_bf16_f32 v4, v4, v5
	v_cvt_pk_bf16_f32 v5, v2, v3
	global_store_dwordx2 v[16:17], v[4:5], off offset:288
	s_waitcnt lgkmcnt(0)
	v_add_f32_e32 v0, v0, v1
	ds_bpermute_b32 v1, v151, v0
	s_and_saveexec_b64 s[2:3], s[36:37]
	s_cbranch_execz .LBB0_872
	s_add_u32 s4, s6, s24
	s_addc_u32 s5, s7, s25
	v_lshl_add_u64 v[2:3], v[138:139], 2, s[4:5]
	s_waitcnt lgkmcnt(0)
	v_add_f32_e32 v0, v0, v1
	global_store_dword v[2:3], v0, off offset:704
